# strategy 2 (prologue de-serialisation): attention q-block prologue issues the ring barrier + first K/V tile LDS-DMA right after the Q loads (offset arithmetic replicated on dead VGPRs) so its flight o
# speedup vs baseline: 1.0021x; 1.0021x over previous
.LBB0_804:
	s_bfe_u32 s0, s66, 0x20001
	s_bfe_u32 s1, s78, 0x10007
	s_lshl_b32 s12, s1, 8
	s_lshl_b32 s44, s0, 9
	s_or_b32 s48, s44, s12
	s_mulk_i32 s0, 0x180
	s_mul_i32 s12, s1, 0xc0
	s_add_i32 s0, s0, s12
	s_lshl_b32 s50, s0, 1
	s_ashr_i32 s0, s78, 4
	s_lshl_b32 s12, s78, 1
	s_and_b32 s0, s0, -16
	s_and_b32 s44, s12, 8
	s_bfe_u32 s80, s78, 0x40003
	s_or_b32 s0, s0, s44
	s_xor_b32 s49, s80, 31
	s_ashr_i32 s0, s0, 3
	s_and_b32 s12, s12, 6
	s_lshl_b32 s83, s49, 8
	s_or_b32 s46, s12, s1
	s_ashr_i32 s1, s0, 31
	s_add_i32 s84, s83, s63
	s_lshr_b32 s81, s78, 3
	v_mov_b32_e32 v172, v1
	s_lshl_b64 s[52:53], s[0:1], 13
	s_ashr_i32 s12, s84, 31
	s_add_u32 s54, s52, s84
	v_and_b32_e32 v168, 31, v172
	v_or_b32_e32 v38, s54, v168
	s_addc_u32 s55, s53, s12
	v_mad_u64_u32 v[2:3], s[44:45], v38, s68, v[146:147]
	s_mul_i32 s82, s46, 0xc0
	v_bfe_u32 v173, v172, 5, 1
	v_mad_i32_i24 v3, s55, v162, v3
	s_lshl_b32 s12, s82, 1
	v_lshl_add_u64 v[2:3], v[2:3], 0, s[12:13]
	v_lshlrev_b32_e32 v148, 4, v173
	v_lshl_add_u64 v[40:41], v[2:3], 0, v[148:149]
	global_load_dwordx4 v[6:9], v[40:41], off
	global_load_dwordx4 v[14:17], v[40:41], off offset:32
	global_load_dwordx4 v[30:33], v[40:41], off offset:64
	global_load_dwordx4 v[34:37], v[40:41], off offset:96
	global_load_dwordx4 v[50:53], v[40:41], off offset:128
	global_load_dwordx4 v[26:29], v[40:41], off offset:160
	global_load_dwordx4 v[22:25], v[40:41], off offset:192
	global_load_dwordx4 v[18:21], v[40:41], off offset:224
	global_load_dwordx4 v[10:13], v[40:41], off offset:256
	global_load_dwordx4 v[42:45], v[40:41], off offset:288
	s_waitcnt lgkmcnt(0)
	global_load_dwordx4 v[2:5], v[40:41], off offset:320
	global_load_dwordx4 v[46:49], v[40:41], off offset:352
	v_and_b32_e32 v40, 32, v172
	v_mov_b32_e32 v39, s55
	s_mul_i32 s86, s0, 0x1800000
	s_mul_hi_i32 s51, s0, 0x1800000
	s_add_u32 s44, s33, s86
	s_addc_u32 s45, s58, s51
	s_lshl_b64 s[56:57], s[0:1], 24
	s_lshl_b32 s79, s46, 7
	s_add_u32 s44, s44, s12
	s_addc_u32 s45, s45, 0
	s_mov_b32 m0, s71
	s_add_u32 s0, s59, s56
	s_addc_u32 s1, s60, s57
	s_lshl_b32 s12, s46, 8
	s_add_u32 s46, s0, s12
	s_addc_u32 s47, s1, 0
	s_lshl_b32 s85, s49, 2
	s_add_i32 s85, s85, 4
	s_or_b32 s48, s56, s48
	s_add_u32 s48, s48, 0x29020000
	s_addc_u32 s49, s57, 0
	s_or_b32 s50, s86, s50
	s_add_u32 s50, s50, 0x23030000
	s_addc_u32 s51, s51, 0
	s_mov_b32 s12, 1
	s_movk_i32 s86, 0xff00
	v_mul_hi_i32 v150, v172, s70
	v_lshrrev_b32_e32 v151, 31, v150
	v_ashrrev_i32_e32 v150, 2, v150
	v_add_u32_e32 v150, v150, v151
	v_mul_lo_u32 v151, v150, 24
	v_sub_u32_e32 v151, v172, v151
	v_lshrrev_b32_e32 v152, 1, v150
	v_bitop3_b32 v151, v152, v151, 7 bitop3:0x6c
	v_mul_lo_u32 v150, v150, s68
	v_lshl_add_u32 v150, v151, 4, v150
	v_add_u32_e32 v151, 0x200, v172
	v_mul_hi_i32 v153, v151, s70
	v_lshrrev_b32_e32 v154, 31, v153
	v_ashrrev_i32_e32 v153, 2, v153
	v_add_u32_e32 v153, v153, v154
	v_mul_lo_u32 v154, v153, 24
	v_sub_u32_e32 v154, v151, v154
	v_lshrrev_b32_e32 v152, 1, v153
	v_bitop3_b32 v154, v152, v154, 7 bitop3:0x6c
	v_mul_lo_u32 v153, v153, s68
	v_lshl_add_u32 v153, v154, 4, v153
	v_add_u32_e32 v154, 0x400, v172
	v_mul_hi_i32 v155, v154, s70
	v_lshrrev_b32_e32 v156, 31, v155
	v_ashrrev_i32_e32 v155, 2, v155
	v_add_u32_e32 v155, v155, v156
	v_mul_lo_u32 v156, v155, 24
	v_sub_u32_e32 v154, v154, v156
	v_lshrrev_b32_e32 v152, 1, v155
	v_bitop3_b32 v154, v152, v154, 7 bitop3:0x6c
	v_mul_lo_u32 v155, v155, s68
	v_ashrrev_i32_e32 v157, 4, v172
	v_lshl_add_u32 v155, v154, 4, v155
	v_bfe_u32 v154, v172, 2, 2
	v_lshrrev_b32_e32 v156, 1, v172
	v_and_b32_e32 v158, 0x1ffff0, v157
	v_lshrrev_b32_e32 v157, 1, v157
	v_ashrrev_i32_e32 v151, 4, v151
	v_and_or_b32 v154, v156, 8, v154
	v_and_b32_e32 v156, 0x60, v172
	v_lshlrev_b32_e32 v159, 3, v172
	v_and_b32_e32 v157, 4, v157
	v_and_b32_e32 v160, 0x1ffff0, v151
	v_lshrrev_b32_e32 v151, 1, v151
	v_and_or_b32 v156, v159, 24, v156
	v_or3_b32 v157, v158, v157, v154
	v_and_b32_e32 v151, 4, v151
	s_barrier
	global_load_lds_dwordx4 v150, s[44:45]
	s_mov_b32 m0, s72
	v_lshlrev_b32_e32 v156, 1, v156
	v_lshlrev_b32_e32 v158, 11, v157
	v_or3_b32 v151, v160, v151, v154
	global_load_lds_dwordx4 v153, s[44:45]
	s_mov_b32 m0, s73
	v_or_b32_e32 v157, v158, v156
	v_lshlrev_b32_e32 v160, 11, v151
	global_load_lds_dwordx4 v155, s[44:45]
	s_mov_b32 m0, s64
	v_or_b32_e32 v151, v160, v156
	global_load_lds_dwordx4 v157, s[46:47]
	s_mov_b32 m0, s74
	v_lshlrev_b32_e32 v161, 1, v172
	global_load_lds_dwordx4 v151, s[46:47]
	s_waitcnt vmcnt(0)
	v_lshlrev_b32_e32 v227, 16, v26
	v_lshlrev_b32_e32 v177, 16, v6
	v_and_b32_e32 v174, 0xffff0000, v6
	v_lshlrev_b32_e32 v170, 16, v7
	v_and_b32_e32 v167, 0xffff0000, v7
	v_lshlrev_b32_e32 v180, 16, v8
	v_and_b32_e32 v176, 0xffff0000, v8
	v_lshlrev_b32_e32 v171, 16, v9
	v_and_b32_e32 v169, 0xffff0000, v9
	v_lshlrev_b32_e32 v185, 16, v14
	v_and_b32_e32 v182, 0xffff0000, v14
	v_lshlrev_b32_e32 v179, 16, v15
	v_and_b32_e32 v175, 0xffff0000, v15
	v_lshlrev_b32_e32 v187, 16, v16
	v_and_b32_e32 v183, 0xffff0000, v16
	v_lshlrev_b32_e32 v181, 16, v17
	v_and_b32_e32 v178, 0xffff0000, v17
	v_lshlrev_b32_e32 v201, 16, v34
	v_and_b32_e32 v198, 0xffff0000, v34
	v_lshlrev_b32_e32 v196, 16, v35
	v_and_b32_e32 v192, 0xffff0000, v35
	v_lshlrev_b32_e32 v202, 16, v36
	v_and_b32_e32 v199, 0xffff0000, v36
	v_lshlrev_b32_e32 v197, 16, v37
	v_and_b32_e32 v194, 0xffff0000, v37
	v_and_b32_e32 v228, 0xffff0000, v26
	global_load_dwordx4 v[142:145], v40, s[4:5] offset:704
	global_load_dwordx4 v[130:133], v40, s[4:5] offset:720
	global_load_dwordx4 v[6:9], v40, s[4:5] offset:592
	v_lshlrev_b32_e32 v229, 16, v27
	global_load_dwordx4 v[14:17], v40, s[4:5] offset:576
	v_and_b32_e32 v230, 0xffff0000, v27
	v_lshlrev_b32_e32 v231, 16, v28
	v_and_b32_e32 v232, 0xffff0000, v28
	v_lshlrev_b32_e32 v233, 16, v29
	v_and_b32_e32 v234, 0xffff0000, v29
	global_load_dwordx4 v[34:37], v40, s[4:5] offset:640
	global_load_dwordx4 v[156:159], v40, s[4:5] offset:656
	global_load_dwordx4 v[26:29], v40, s[4:5] offset:528
	v_mul_f32_e32 v209, v174, v174
	v_fmac_f32_e32 v209, v177, v177
	v_fmac_f32_e32 v209, v170, v170
	v_fmac_f32_e32 v209, v167, v167
	v_fmac_f32_e32 v209, v180, v180
	v_fmac_f32_e32 v209, v176, v176
	v_fmac_f32_e32 v209, v171, v171
	v_fmac_f32_e32 v209, v169, v169
	v_fmac_f32_e32 v209, v185, v185
	v_lshlrev_b32_e32 v193, 16, v30
	v_and_b32_e32 v190, 0xffff0000, v30
	v_lshlrev_b32_e32 v188, 16, v31
	v_and_b32_e32 v184, 0xffff0000, v31
	v_lshlrev_b32_e32 v195, 16, v32
	v_and_b32_e32 v191, 0xffff0000, v32
	v_lshlrev_b32_e32 v189, 16, v33
	v_and_b32_e32 v186, 0xffff0000, v33
	v_fmac_f32_e32 v209, v182, v182
	global_load_dwordx4 v[30:33], v40, s[4:5] offset:512
	v_fmac_f32_e32 v209, v179, v179
	v_fmac_f32_e32 v209, v175, v175
	v_fmac_f32_e32 v209, v187, v187
	v_fmac_f32_e32 v209, v183, v183
	v_fmac_f32_e32 v209, v181, v181
	v_fmac_f32_e32 v209, v178, v178
	v_fmac_f32_e32 v209, v193, v193
	v_fmac_f32_e32 v209, v190, v190
	v_fmac_f32_e32 v209, v188, v188
	v_fmac_f32_e32 v209, v184, v184
	v_fmac_f32_e32 v209, v195, v195
	v_fmac_f32_e32 v209, v191, v191
	v_fmac_f32_e32 v209, v189, v189
	v_fmac_f32_e32 v209, v186, v186
	v_fmac_f32_e32 v209, v201, v201
	v_fmac_f32_e32 v209, v198, v198
	v_fmac_f32_e32 v209, v196, v196
	v_fmac_f32_e32 v209, v192, v192
	v_fmac_f32_e32 v209, v202, v202
	v_fmac_f32_e32 v209, v199, v199
	v_fmac_f32_e32 v209, v197, v197
	v_lshlrev_b32_e32 v207, 16, v50
	v_fmac_f32_e32 v209, v194, v194
	v_and_b32_e32 v205, 0xffff0000, v50
	v_fmac_f32_e32 v209, v207, v207
	v_lshlrev_b32_e32 v203, 16, v51
	v_fmac_f32_e32 v209, v205, v205
	v_and_b32_e32 v200, 0xffff0000, v51
	v_fmac_f32_e32 v209, v203, v203
	v_lshlrev_b32_e32 v208, 16, v52
	v_fmac_f32_e32 v209, v200, v200
	v_and_b32_e32 v206, 0xffff0000, v52
	v_fmac_f32_e32 v209, v208, v208
	v_lshlrev_b32_e32 v204, 16, v53
	v_fmac_f32_e32 v209, v206, v206
	v_and_b32_e32 v226, 0xffff0000, v53
	v_fmac_f32_e32 v209, v204, v204
	v_fmac_f32_e32 v209, v226, v226
	v_fmac_f32_e32 v209, v227, v227
	v_fmac_f32_e32 v209, v228, v228
	v_fmac_f32_e32 v209, v229, v229
	v_fmac_f32_e32 v209, v230, v230
	global_load_dwordx4 v[110:113], v40, s[4:5] offset:16
	global_load_dwordx4 v[114:117], v40, s[4:5]
	global_load_dwordx4 v[102:105], v40, s[4:5] offset:80
	global_load_dwordx4 v[106:109], v40, s[4:5] offset:64
	global_load_dwordx4 v[94:97], v40, s[4:5] offset:144
	global_load_dwordx4 v[98:101], v40, s[4:5] offset:128
	global_load_dwordx4 v[86:89], v40, s[4:5] offset:208
	global_load_dwordx4 v[90:93], v40, s[4:5] offset:192
	global_load_dwordx4 v[78:81], v40, s[4:5] offset:272
	global_load_dwordx4 v[82:85], v40, s[4:5] offset:256
	global_load_dwordx4 v[70:73], v40, s[4:5] offset:336
	global_load_dwordx4 v[74:77], v40, s[4:5] offset:320
	global_load_dwordx4 v[62:65], v40, s[4:5] offset:400
	global_load_dwordx4 v[66:69], v40, s[4:5] offset:384
	global_load_dwordx4 v[54:57], v40, s[4:5] offset:464
	global_load_dwordx4 v[58:61], v40, s[4:5] offset:448
	v_fmac_f32_e32 v209, v231, v231
	v_fmac_f32_e32 v209, v232, v232
	v_fmac_f32_e32 v209, v233, v233
	v_fmac_f32_e32 v209, v234, v234
	s_waitcnt vmcnt(29)
	v_lshlrev_b32_e32 v235, 16, v22
	v_and_b32_e32 v236, 0xffff0000, v22
	v_fmac_f32_e32 v209, v235, v235
	v_lshlrev_b32_e32 v237, 16, v23
	v_fmac_f32_e32 v209, v236, v236
	v_and_b32_e32 v238, 0xffff0000, v23
	v_fmac_f32_e32 v209, v237, v237
	v_lshlrev_b32_e32 v239, 16, v24
	v_fmac_f32_e32 v209, v238, v238
	v_and_b32_e32 v240, 0xffff0000, v24
	v_fmac_f32_e32 v209, v239, v239
	v_lshlrev_b32_e32 v241, 16, v25
	v_fmac_f32_e32 v209, v240, v240
	v_and_b32_e32 v242, 0xffff0000, v25
	v_fmac_f32_e32 v209, v241, v241
	v_fmac_f32_e32 v209, v242, v242
	s_waitcnt vmcnt(28)
	v_lshlrev_b32_e32 v243, 16, v18
	v_and_b32_e32 v244, 0xffff0000, v18
	v_fmac_f32_e32 v209, v243, v243
	v_lshlrev_b32_e32 v245, 16, v19
	v_fmac_f32_e32 v209, v244, v244
	v_and_b32_e32 v246, 0xffff0000, v19
	v_fmac_f32_e32 v209, v245, v245
	v_lshlrev_b32_e32 v247, 16, v20
	v_fmac_f32_e32 v209, v246, v246
	v_and_b32_e32 v248, 0xffff0000, v20
	v_fmac_f32_e32 v209, v247, v247
	v_lshlrev_b32_e32 v249, 16, v21
	v_fmac_f32_e32 v209, v248, v248
	v_and_b32_e32 v250, 0xffff0000, v21
	v_fmac_f32_e32 v209, v249, v249
	s_waitcnt vmcnt(27)
	v_lshlrev_b32_e32 v223, 16, v10
	s_waitcnt vmcnt(25)
	v_lshlrev_b32_e32 v222, 16, v2
	v_fmac_f32_e32 v209, v250, v250
	s_waitcnt vmcnt(18)
	v_mov_b32_e32 v150, v158
	v_mov_b32_e32 v158, v156
	v_lshlrev_b32_e32 v156, 16, v3
	v_and_b32_e32 v160, 0xffff0000, v3
	v_and_b32_e32 v225, 0xffff0000, v10
	v_and_b32_e32 v224, 0xffff0000, v2
	v_mul_f32_e32 v2, v222, v222
	v_mul_f32_e32 v3, v223, v223
	v_mov_b32_e32 v134, v144
	v_mov_b32_e32 v140, v142
	v_lshlrev_b32_e32 v142, 16, v5
	s_waitcnt vmcnt(17)
	v_mov_b32_e32 v151, v28
	v_and_b32_e32 v144, 0xffff0000, v5
	v_mov_b32_e32 v28, v159
	v_lshlrev_b32_e32 v152, 16, v4
	v_mov_b32_e32 v159, v26
	v_and_b32_e32 v154, 0xffff0000, v4
	v_mov_b32_e32 v26, v157
	v_lshlrev_b32_e32 v157, 16, v11
	v_add_f32_e32 v3, v3, v209
	v_mul_f32_e32 v4, v224, v224
	v_mul_f32_e32 v5, v225, v225
	v_lshlrev_b32_e32 v119, 16, v45
	v_and_b32_e32 v121, 0xffff0000, v45
	v_lshlrev_b32_e32 v125, 16, v44
	v_and_b32_e32 v127, 0xffff0000, v44
	v_mul_f32_e32 v44, v156, v156
	v_mul_f32_e32 v45, v157, v157
	v_and_b32_e32 v161, 0xffff0000, v11
	v_add_f32_e32 v3, v5, v3
	v_mov_b32_e32 v122, v132
	v_mov_b32_e32 v128, v130
	v_lshlrev_b32_e32 v130, 16, v47
	v_and_b32_e32 v132, 0xffff0000, v47
	v_lshlrev_b32_e32 v136, 16, v46
	v_and_b32_e32 v138, 0xffff0000, v46
	v_lshlrev_b32_e32 v153, 16, v12
	v_mul_f32_e32 v46, v160, v160
	v_mul_f32_e32 v47, v161, v161
	v_add_f32_e32 v3, v45, v3
	v_mov_b32_e32 v123, v8
	v_mov_b32_e32 v8, v133
	v_mov_b32_e32 v129, v6
	v_mov_b32_e32 v6, v131
	v_lshlrev_b32_e32 v131, 16, v43
	v_and_b32_e32 v133, 0xffff0000, v43
	v_lshlrev_b32_e32 v137, 16, v42
	v_and_b32_e32 v139, 0xffff0000, v42
	v_mul_f32_e32 v42, v152, v152
	v_mul_f32_e32 v43, v153, v153
	v_and_b32_e32 v155, 0xffff0000, v12
	v_add_f32_e32 v3, v47, v3
	v_mov_b32_e32 v141, v14
	v_mov_b32_e32 v14, v143
	v_lshlrev_b32_e32 v143, 16, v13
	v_mul_f32_e32 v220, v154, v154
	v_mul_f32_e32 v221, v155, v155
	v_add_f32_e32 v3, v43, v3
	v_mov_b32_e32 v135, v16
	v_mov_b32_e32 v16, v145
	v_mul_f32_e32 v216, v142, v142
	v_mul_f32_e32 v217, v143, v143
	v_and_b32_e32 v145, 0xffff0000, v13
	v_add_f32_e32 v3, v221, v3
	v_mul_f32_e32 v218, v144, v144
	v_mul_f32_e32 v219, v145, v145
	v_add_f32_e32 v3, v217, v3
	v_mul_f32_e32 v212, v136, v136
	v_mul_f32_e32 v213, v137, v137
	v_add_f32_e32 v3, v219, v3
	v_mul_f32_e32 v214, v138, v138
	v_mul_f32_e32 v215, v139, v139
	v_add_f32_e32 v3, v213, v3
	v_add_f32_e32 v3, v215, v3
	v_fmac_f32_e32 v3, v131, v131
	v_fmac_f32_e32 v3, v133, v133
	v_fmac_f32_e32 v3, v125, v125
	v_fmac_f32_e32 v3, v127, v127
	v_fmac_f32_e32 v3, v119, v119
	v_fmac_f32_e32 v3, v121, v121
	v_add_f32_e32 v2, v2, v3
	v_add_f32_e32 v43, v4, v2
	v_add_f32_e32 v43, v44, v43
	v_add_f32_e32 v43, v46, v43
	v_add_f32_e32 v209, v42, v43
	v_add_f32_e32 v209, v220, v209
	v_add_f32_e32 v209, v216, v209
	v_add_f32_e32 v209, v218, v209
	v_mov_b32_e32 v218, v132
	v_mov_b32_e32 v219, v130
	v_add_f32_e32 v209, v212, v209
	v_lshlrev_b64 v[18:19], 8, v[38:39]
	v_lshlrev_b32_e32 v124, 16, v48
	v_and_b32_e32 v126, 0xffff0000, v48
	v_mul_f32_e32 v218, v218, v218
	v_mul_f32_e32 v219, v219, v219
	s_waitcnt vmcnt(16)
	v_mov_b32_e32 v213, v32
	v_add_f32_e32 v32, v214, v209
	v_lshl_add_u64 v[18:19], s[10:11], 0, v[18:19]
	v_lshlrev_b32_e32 v20, 6, v173
	v_mov_b32_e32 v21, v149
	v_mov_b32_e32 v216, v126
	v_mov_b32_e32 v217, v124
	v_add_f32_e32 v32, v219, v32
	v_lshl_add_u64 v[210:211], v[18:19], 0, v[20:21]
	v_lshlrev_b32_e32 v118, 16, v49
	v_and_b32_e32 v120, 0xffff0000, v49
	v_mul_f32_e32 v216, v216, v216
	v_mul_f32_e32 v217, v217, v217
	v_add_f32_e32 v32, v218, v32
	global_load_dwordx4 v[18:21], v[210:211], off offset:48
	global_load_dwordx4 v[22:25], v[210:211], off offset:32
	global_load_dwordx4 v[38:41], v[210:211], off offset:16
	global_load_dwordx4 v[50:53], v[210:211], off
	global_load_dwordx4 v[2:5], v[210:211], off offset:176
	global_load_dwordx4 v[10:13], v[210:211], off offset:160
	global_load_dwordx4 v[42:45], v[210:211], off offset:144
	global_load_dwordx4 v[46:49], v[210:211], off offset:128
	v_mov_b32_e32 v210, v120
	v_mov_b32_e32 v211, v118
	v_add_f32_e32 v32, v217, v32
	v_mul_f32_e32 v210, v210, v210
	v_mul_f32_e32 v211, v211, v211
	v_add_f32_e32 v32, v216, v32
	v_add_f32_e32 v32, v211, v32
	v_add_f32_e32 v32, v210, v32
	v_mov_b32_e32 v212, v36
	v_mov_b32_e32 v36, v32
	s_nop 1
	v_permlane32_swap_b32_e32 v32, v36
	v_add_f32_e32 v32, v32, v36
	v_fmamk_f32 v32, v32, 0x3baaaaab, v163
	v_mul_f32_e32 v36, 0x4b800000, v32
	v_cmp_gt_f32_e32 vcc, s69, v32
	s_nop 1
	v_cndmask_b32_e32 v32, v32, v36, vcc
	v_rsq_f32_e32 v209, v32
	v_mov_b32_e32 v32, v37
	v_mov_b32_e32 v37, v30
	v_mov_b32_e32 v36, v34
	v_mul_f32_e32 v30, 0x45800000, v209
	v_cndmask_b32_e32 v30, v209, v30, vcc
	v_mul_f32_e32 v34, 0x3dd53b94, v30
	s_waitcnt vmcnt(22)
	v_mul_f32_e32 v30, v114, v34
	v_mul_f32_e32 v114, v30, v177
	v_mul_f32_e32 v30, v110, v34
	v_mul_f32_e32 v110, v30, v180
	v_mul_f32_e32 v30, v115, v34
	v_mul_f32_e32 v115, v30, v174
	v_mul_f32_e32 v30, v111, v34
	v_mul_f32_e32 v111, v30, v176
	v_mul_f32_e32 v30, v116, v34
	v_mul_f32_e32 v116, v30, v170
	v_mul_f32_e32 v30, v112, v34
	v_mul_f32_e32 v112, v30, v171
	v_mul_f32_e32 v30, v117, v34
	v_mul_f32_e32 v117, v30, v167
	v_mul_f32_e32 v30, v113, v34
	v_mul_f32_e32 v113, v30, v169
	s_waitcnt vmcnt(20)
	v_mul_f32_e32 v30, v106, v34
	v_mul_f32_e32 v106, v30, v185
	v_mul_f32_e32 v30, v102, v34
	v_mul_f32_e32 v167, v30, v187
	v_mul_f32_e32 v30, v107, v34
	v_mul_f32_e32 v102, v30, v182
	v_mul_f32_e32 v30, v103, v34
	v_mul_f32_e32 v107, v30, v183
	v_mul_f32_e32 v30, v108, v34
	v_mul_f32_e32 v103, v30, v179
	v_mul_f32_e32 v30, v104, v34
	v_mul_f32_e32 v108, v30, v181
	v_mul_f32_e32 v30, v109, v34
	v_mul_f32_e32 v104, v30, v175
	v_mul_f32_e32 v30, v105, v34
	v_mul_f32_e32 v105, v30, v178
	s_waitcnt vmcnt(18)
	v_mul_f32_e32 v30, v98, v34
	v_mul_f32_e32 v109, v30, v193
	v_mul_f32_e32 v30, v94, v34
	v_mul_f32_e32 v94, v30, v195
	v_mul_f32_e32 v30, v99, v34
	v_mul_f32_e32 v169, v30, v190
	v_mul_f32_e32 v30, v95, v34
	v_mul_f32_e32 v95, v30, v191
	v_mul_f32_e32 v30, v100, v34
	v_mul_f32_e32 v170, v30, v188
	v_mul_f32_e32 v30, v96, v34
	v_mul_f32_e32 v96, v30, v189
	v_mul_f32_e32 v30, v101, v34
	v_mul_f32_e32 v171, v30, v184
	v_mul_f32_e32 v30, v97, v34
	v_mul_f32_e32 v97, v30, v186
	s_waitcnt vmcnt(16)
	v_mul_f32_e32 v30, v90, v34
	v_mul_f32_e32 v90, v30, v201
	v_mul_f32_e32 v30, v86, v34
	v_mul_f32_e32 v86, v30, v202
	v_mul_f32_e32 v30, v91, v34
	v_mul_f32_e32 v91, v30, v198
	v_mul_f32_e32 v30, v87, v34
	v_mul_f32_e32 v87, v30, v199
	v_mul_f32_e32 v30, v92, v34
	v_mul_f32_e32 v92, v30, v196
	v_mul_f32_e32 v30, v88, v34
	v_mul_f32_e32 v88, v30, v197
	v_mul_f32_e32 v30, v93, v34
	v_mul_f32_e32 v93, v30, v192
	v_mul_f32_e32 v30, v89, v34
	v_mul_f32_e32 v89, v30, v194
	s_waitcnt vmcnt(14)
	v_mul_f32_e32 v30, v82, v34
	v_mul_f32_e32 v82, v30, v207
	v_mul_f32_e32 v30, v34, v78
	v_mul_f32_e32 v78, v30, v208
	v_mul_f32_e32 v30, v83, v34
	v_mul_f32_e32 v83, v30, v205
	v_mul_f32_e32 v30, v34, v79
	v_mul_f32_e32 v79, v30, v206
	v_mul_f32_e32 v30, v84, v34
	v_mul_f32_e32 v84, v30, v203
	v_mul_f32_e32 v30, v34, v80
	v_mul_f32_e32 v80, v30, v204
	v_mul_f32_e32 v30, v85, v34
	v_mul_f32_e32 v85, v30, v200
	v_mul_f32_e32 v30, v34, v81
	v_mul_f32_e32 v81, v30, v226
	s_waitcnt vmcnt(12)
	v_mul_f32_e32 v30, v34, v74
	v_mul_f32_e32 v74, v30, v227
	v_mul_f32_e32 v30, v34, v70
	v_mul_f32_e32 v70, v30, v231
	v_mul_f32_e32 v30, v34, v75
	v_mul_f32_e32 v75, v30, v228
	v_mul_f32_e32 v30, v34, v71
	v_mul_f32_e32 v71, v30, v232
	v_mul_f32_e32 v30, v34, v76
	v_mul_f32_e32 v76, v30, v229
	v_mul_f32_e32 v30, v34, v72
	v_mul_f32_e32 v72, v30, v233
	v_mul_f32_e32 v30, v34, v77
	v_mul_f32_e32 v77, v30, v230
	v_mul_f32_e32 v30, v34, v73
	v_mul_f32_e32 v73, v30, v234
	s_waitcnt vmcnt(10)
	v_mul_f32_e32 v30, v34, v66
	v_mul_f32_e32 v174, v30, v235
	v_mul_f32_e32 v30, v34, v62
	v_mul_f32_e32 v175, v30, v239
	v_mul_f32_e32 v30, v34, v67
	v_mul_f32_e32 v176, v30, v236
	v_mul_f32_e32 v30, v34, v63
	v_mul_f32_e32 v177, v30, v240
	v_mul_f32_e32 v30, v34, v68
	v_mul_f32_e32 v68, v30, v237
	v_mul_f32_e32 v30, v34, v64
	v_mul_f32_e32 v178, v30, v241
	v_mul_f32_e32 v30, v34, v69
	v_mul_f32_e32 v69, v30, v238
	v_mul_f32_e32 v30, v34, v65
	v_mul_f32_e32 v179, v30, v242
	s_waitcnt vmcnt(8)
	v_mul_f32_e32 v30, v34, v58
	v_mul_f32_e32 v180, v30, v243
	v_mul_f32_e32 v30, v34, v54
	v_mul_f32_e32 v181, v30, v247
	v_mul_f32_e32 v30, v34, v59
	v_mul_f32_e32 v182, v30, v244
	v_mul_f32_e32 v30, v34, v55
	v_mul_f32_e32 v183, v30, v248
	v_mul_f32_e32 v30, v34, v60
	v_mul_f32_e32 v184, v30, v245
	v_mul_f32_e32 v30, v34, v56
	v_mul_f32_e32 v185, v30, v249
	v_mul_f32_e32 v30, v34, v61
	v_mul_f32_e32 v186, v30, v246
	v_mul_f32_e32 v30, v34, v57
	v_mul_f32_e32 v36, v34, v36
	v_mul_f32_e32 v37, v34, v37
	v_mul_f32_e32 v187, v30, v250
	v_mul_f32_e32 v36, v36, v222
	v_mul_f32_e32 v37, v37, v223
	v_mov_b32_e32 v30, v35
	v_mul_f32_e32 v54, v34, v158
	v_mul_f32_e32 v55, v34, v159
	v_mul_f32_e32 v30, v34, v30
	v_mul_f32_e32 v31, v34, v31
	v_mul_f32_e32 v26, v34, v26
	v_mul_f32_e32 v27, v34, v27
	v_mul_f32_e32 v56, v34, v212
	v_mul_f32_e32 v57, v34, v213
	v_mul_f32_e32 v58, v34, v150
	v_mul_f32_e32 v59, v34, v151
	v_mul_f32_e32 v32, v34, v32
	v_mul_f32_e32 v33, v34, v33
	v_mul_f32_e32 v28, v34, v28
	v_mul_f32_e32 v29, v34, v29
	v_mul_f32_e32 v60, v34, v140
	v_mul_f32_e32 v61, v34, v141
	v_mul_f32_e32 v62, v34, v128
	v_mul_f32_e32 v63, v34, v129
	v_mul_f32_e32 v14, v34, v14
	v_mul_f32_e32 v15, v34, v15
	v_mul_f32_e32 v6, v34, v6
	v_mul_f32_e32 v7, v34, v7
	v_mul_f32_e32 v64, v34, v134
	v_mul_f32_e32 v65, v34, v135
	v_mul_f32_e32 v66, v34, v122
	v_mul_f32_e32 v67, v34, v123
	v_mul_f32_e32 v16, v34, v16
	v_mul_f32_e32 v17, v34, v17
	v_mul_f32_e32 v8, v34, v8
	v_mul_f32_e32 v9, v34, v9
	s_waitcnt vmcnt(4)
	v_mul_f32_e32 v34, v37, v50
	v_mul_f32_e32 v35, v36, v51
	v_mul_f32_e32 v30, v30, v224
	v_mul_f32_e32 v31, v31, v225
	v_mul_f32_e32 v64, v64, v130
	v_mul_f32_e32 v65, v65, v131
	v_sub_f32_e32 v130, v34, v35
	v_mul_f32_e32 v34, v36, v50
	v_mul_f32_e32 v35, v37, v51
	v_mul_f32_e32 v56, v56, v156
	v_mul_f32_e32 v57, v57, v157
	v_add_f32_e32 v36, v35, v34
	v_mul_f32_e32 v34, v31, v52
	v_mul_f32_e32 v35, v30, v53
	v_mul_f32_e32 v30, v30, v52
	v_mul_f32_e32 v31, v31, v53
	v_sub_f32_e32 v34, v34, v35
	v_add_f32_e32 v35, v31, v30
	v_mul_f32_e32 v30, v57, v38
	v_mul_f32_e32 v31, v56, v39
	v_mul_f32_e32 v32, v32, v160
	v_mul_f32_e32 v33, v33, v161
	v_sub_f32_e32 v37, v30, v31
	v_mul_f32_e32 v30, v56, v38
	v_mul_f32_e32 v31, v57, v39
	v_mul_f32_e32 v54, v54, v152
	v_mul_f32_e32 v55, v55, v153
	v_add_f32_e32 v38, v31, v30
	v_mul_f32_e32 v30, v33, v40
	v_mul_f32_e32 v31, v32, v41
	v_sub_f32_e32 v39, v30, v31
	v_mul_f32_e32 v30, v32, v40
	v_mul_f32_e32 v31, v33, v41
	v_mul_f32_e32 v26, v26, v154
	v_mul_f32_e32 v27, v27, v155
	v_add_f32_e32 v32, v31, v30
	v_mul_f32_e32 v30, v55, v22
	v_mul_f32_e32 v31, v54, v23
	v_mul_f32_e32 v22, v54, v22
	v_mul_f32_e32 v23, v55, v23
	v_sub_f32_e32 v30, v30, v31
	v_add_f32_e32 v31, v23, v22
	v_mul_f32_e32 v22, v27, v24
	v_mul_f32_e32 v23, v26, v25
	v_mul_f32_e32 v58, v58, v142
	v_mul_f32_e32 v59, v59, v143
	v_sub_f32_e32 v33, v22, v23
	v_mul_f32_e32 v22, v26, v24
	v_mul_f32_e32 v23, v27, v25
	v_mul_f32_e32 v28, v28, v144
	v_mul_f32_e32 v29, v29, v145
	v_add_f32_e32 v24, v23, v22
	v_mul_f32_e32 v22, v59, v18
	v_mul_f32_e32 v23, v58, v19
	v_mul_f32_e32 v18, v58, v18
	v_mul_f32_e32 v19, v59, v19
	v_sub_f32_e32 v22, v22, v23
	v_add_f32_e32 v23, v19, v18
	v_mul_f32_e32 v18, v29, v20
	v_mul_f32_e32 v19, v28, v21
	v_mul_f32_e32 v60, v60, v136
	v_mul_f32_e32 v61, v61, v137
	v_sub_f32_e32 v25, v18, v19
	v_mul_f32_e32 v18, v28, v20
	v_mul_f32_e32 v19, v29, v21
	v_mul_f32_e32 v14, v14, v138
	v_mul_f32_e32 v15, v15, v139
	v_add_f32_e32 v20, v19, v18
	s_waitcnt vmcnt(0)
	v_mul_f32_e32 v18, v61, v46
	v_mul_f32_e32 v19, v60, v47
	v_sub_f32_e32 v21, v18, v19
	v_mul_f32_e32 v18, v60, v46
	v_mul_f32_e32 v19, v61, v47
	v_mul_f32_e32 v16, v16, v132
	v_mul_f32_e32 v17, v17, v133
	v_add_f32_e32 v26, v19, v18
	v_mul_f32_e32 v18, v15, v48
	v_mul_f32_e32 v19, v14, v49
	v_mul_f32_e32 v14, v14, v48
	v_mul_f32_e32 v15, v15, v49
	v_sub_f32_e32 v18, v18, v19
	v_add_f32_e32 v19, v15, v14
	v_mul_f32_e32 v14, v65, v42
	v_mul_f32_e32 v15, v64, v43
	v_sub_f32_e32 v27, v14, v15
	v_mul_f32_e32 v14, v64, v42
	v_mul_f32_e32 v15, v65, v43
	v_mul_f32_e32 v62, v62, v124
	v_mul_f32_e32 v63, v63, v125
	v_add_f32_e32 v28, v15, v14
	v_mul_f32_e32 v14, v17, v44
	v_mul_f32_e32 v15, v16, v45
	v_sub_f32_e32 v29, v14, v15
	v_mul_f32_e32 v14, v16, v44
	v_mul_f32_e32 v15, v17, v45
	v_mul_f32_e32 v6, v6, v126
	v_mul_f32_e32 v7, v7, v127
	v_add_f32_e32 v16, v15, v14
	v_mul_f32_e32 v14, v63, v10
	v_mul_f32_e32 v15, v62, v11
	v_mul_f32_e32 v10, v62, v10
	v_mul_f32_e32 v11, v63, v11
	v_mul_f32_e32 v66, v66, v118
	v_mul_f32_e32 v67, v67, v119
	v_sub_f32_e32 v14, v14, v15
	v_add_f32_e32 v15, v11, v10
	v_mul_f32_e32 v10, v7, v12
	v_mul_f32_e32 v11, v6, v13
	v_mul_f32_e32 v6, v6, v12
	v_mul_f32_e32 v7, v7, v13
	v_mul_f32_e32 v8, v8, v120
	v_mul_f32_e32 v9, v9, v121
	v_sub_f32_e32 v10, v10, v11
	v_add_f32_e32 v11, v7, v6
	v_mul_f32_e32 v6, v67, v2
	v_mul_f32_e32 v7, v66, v3
	v_mul_f32_e32 v2, v66, v2
	v_mul_f32_e32 v3, v67, v3
	v_sub_f32_e32 v6, v6, v7
	v_add_f32_e32 v7, v3, v2
	v_mul_f32_e32 v2, v9, v4
	v_mul_f32_e32 v3, v8, v5
	v_sub_f32_e32 v12, v2, v3
	v_mul_f32_e32 v2, v8, v4
	v_mul_f32_e32 v3, v9, v5
	v_cvt_pk_bf16_f32 v98, v114, v115
	v_cvt_pk_bf16_f32 v99, v116, v117
	v_cvt_pk_bf16_f32 v100, v110, v111
	v_cvt_pk_bf16_f32 v101, v112, v113
	v_cvt_pk_bf16_f32 v102, v106, v102
	s_nop 0
	v_add_f32_e32 v2, v3, v2
	v_cvt_pk_bf16_f32 v103, v103, v104
	v_cvt_pk_bf16_f32 v104, v167, v107
	v_cvt_pk_bf16_f32 v105, v108, v105
	v_cvt_pk_bf16_f32 v106, v109, v169
	v_cvt_pk_bf16_f32 v107, v170, v171
	v_cvt_pk_bf16_f32 v108, v94, v95
	v_cvt_pk_bf16_f32 v109, v96, v97
	v_cvt_pk_bf16_f32 v110, v90, v91
	v_cvt_pk_bf16_f32 v111, v92, v93
	v_cvt_pk_bf16_f32 v112, v86, v87
	v_cvt_pk_bf16_f32 v113, v88, v89
	v_cvt_pk_bf16_f32 v114, v82, v83
	v_cvt_pk_bf16_f32 v115, v84, v85
	v_cvt_pk_bf16_f32 v116, v78, v79
	v_cvt_pk_bf16_f32 v117, v80, v81
	v_cvt_pk_bf16_f32 v118, v74, v75
	v_cvt_pk_bf16_f32 v119, v76, v77
	v_cvt_pk_bf16_f32 v120, v70, v71
	v_cvt_pk_bf16_f32 v121, v72, v73
	v_cvt_pk_bf16_f32 v122, v174, v176
	v_cvt_pk_bf16_f32 v123, v68, v69
	v_cvt_pk_bf16_f32 v124, v175, v177
	v_cvt_pk_bf16_f32 v125, v178, v179
	v_cvt_pk_bf16_f32 v126, v180, v182
	v_cvt_pk_bf16_f32 v127, v184, v186
	v_cvt_pk_bf16_f32 v128, v181, v183
	v_cvt_pk_bf16_f32 v129, v185, v187
	v_cvt_pk_bf16_f32 v130, v130, v34
	v_cvt_pk_bf16_f32 v131, v37, v39
	v_cvt_pk_bf16_f32 v132, v30, v33
	v_cvt_pk_bf16_f32 v133, v22, v25
	v_cvt_pk_bf16_f32 v134, v21, v18
	v_cvt_pk_bf16_f32 v135, v27, v29
	v_cvt_pk_bf16_f32 v136, v14, v10
	v_cvt_pk_bf16_f32 v137, v6, v12
	v_cvt_pk_bf16_f32 v138, v36, v35
	v_cvt_pk_bf16_f32 v139, v38, v32
	v_cvt_pk_bf16_f32 v140, v31, v24
	v_cvt_pk_bf16_f32 v141, v23, v20
	v_cvt_pk_bf16_f32 v142, v26, v19
	v_cvt_pk_bf16_f32 v143, v28, v16
	v_cvt_pk_bf16_f32 v144, v15, v11
	v_cvt_pk_bf16_f32 v145, v7, v2
	v_mul_hi_i32 v2, v172, s70
	v_lshrrev_b32_e32 v3, 31, v2
	v_ashrrev_i32_e32 v2, 2, v2
	v_add_u32_e32 v2, v2, v3
	v_mul_lo_u32 v3, v2, 24
	v_sub_u32_e32 v3, v172, v3
	v_lshrrev_b32_e32 v16, 1, v2
	v_bitop3_b32 v3, v16, v3, 7 bitop3:0x6c
	v_mul_lo_u32 v2, v2, s68
	v_lshl_add_u32 v2, v3, 4, v2
	v_add_u32_e32 v3, 0x200, v172
	v_mul_hi_i32 v4, v3, s70
	v_lshrrev_b32_e32 v5, 31, v4
	v_ashrrev_i32_e32 v4, 2, v4
	v_add_u32_e32 v4, v4, v5
	v_mul_lo_u32 v5, v4, 24
	v_sub_u32_e32 v5, v3, v5
	v_lshrrev_b32_e32 v16, 1, v4
	v_bitop3_b32 v5, v16, v5, 7 bitop3:0x6c
	v_mul_lo_u32 v4, v4, s68
	v_lshl_add_u32 v4, v5, 4, v4
	v_add_u32_e32 v5, 0x400, v172
	v_mul_hi_i32 v6, v5, s70
	v_lshrrev_b32_e32 v7, 31, v6
	v_ashrrev_i32_e32 v6, 2, v6
	v_add_u32_e32 v6, v6, v7
	v_mul_lo_u32 v7, v6, 24
	v_sub_u32_e32 v5, v5, v7
	v_lshrrev_b32_e32 v16, 1, v6
	v_bitop3_b32 v5, v16, v5, 7 bitop3:0x6c
	v_mul_lo_u32 v6, v6, s68
	v_ashrrev_i32_e32 v9, 4, v172
	v_lshl_add_u32 v6, v5, 4, v6
	v_bfe_u32 v5, v172, 2, 2
	v_lshrrev_b32_e32 v7, 1, v172
	v_and_b32_e32 v10, 0x1ffff0, v9
	v_lshrrev_b32_e32 v9, 1, v9
	v_ashrrev_i32_e32 v3, 4, v3
	v_and_or_b32 v5, v7, 8, v5
	v_and_b32_e32 v7, 0x60, v172
	v_lshlrev_b32_e32 v8, 3, v172
	v_and_b32_e32 v9, 4, v9
	v_and_b32_e32 v11, 0x1ffff0, v3
	v_lshrrev_b32_e32 v3, 1, v3
	v_and_or_b32 v7, v8, 24, v7
	v_or3_b32 v9, v10, v9, v5
	v_and_b32_e32 v3, 4, v3


	v_lshlrev_b32_e32 v7, 1, v7
	v_lshlrev_b32_e32 v10, 11, v9
	v_or3_b32 v3, v11, v3, v5


	v_or_b32_e32 v9, v10, v7
	v_lshlrev_b32_e32 v11, 11, v3


	v_or_b32_e32 v3, v11, v7


	v_lshlrev_b32_e32 v13, 1, v172

	v_lshlrev_b32_e32 v9, 4, v172
	v_and_b32_e32 v14, 32, v13
	v_or_b32_e32 v3, 32, v148
	v_and_b32_e32 v16, 0x13, v168
	v_and_b32_e32 v17, 4, v168
	v_lshl_or_b32 v16, v17, 1, v16
	v_and_b32_e32 v17, 8, v168
	v_lshrrev_b32_e32 v17, 1, v17
	v_or_b32_e32 v16, v16, v17
	v_mul_u32_u24_e32 v5, 0x180, v16
	v_lshlrev_b32_e32 v17, 3, v16
	v_and_b32_e32 v7, 0x70, v17
	v_and_b32_e32 v12, 0xc0, v9
	v_and_or_b32 v8, v8, s75, v14
	v_and_b32_e32 v167, 63, v172
	v_bitop3_b32 v169, v3, v5, v7 bitop3:0xde
	v_or_b32_e32 v3, 64, v148
	v_add3_u32 v172, v12, 0, v8
	v_and_b32_e32 v12, 0xc0, v13
	v_and_b32_e32 v13, 48, v9
	v_bitop3_b32 v170, v3, v5, v7 bitop3:0xde
	v_or_b32_e32 v3, 0x60, v148
	v_or3_b32 v8, v11, v12, v13
	v_mov_b32_e32 v9, v149
	v_bitop3_b32 v161, v148, v5, v7 bitop3:0xde
	v_bitop3_b32 v171, v3, v5, v7 bitop3:0xde
	v_mov_b32_e32 v3, v149
	v_mov_b32_e32 v5, v149
	v_mov_b32_e32 v7, v149
	v_mul_i32_i24_e32 v15, -8, v173
	v_lshl_add_u64 v[150:151], s[48:49], 0, v[8:9]
	v_mov_b32_e32 v240, v8
	v_or3_b32 v8, v10, v12, v13
	v_mov_b32_e32 v16, v149
	v_mov_b32_e32 v17, v149
	v_lshl_add_u32 v160, v168, 2, s65
	v_lshl_add_u64 v[152:153], s[48:49], 0, v[8:9]
	v_mov_b32_e32 v241, v8
	v_lshl_add_u64 v[154:155], s[50:51], 0, v[6:7]
	v_mov_b32_e32 v242, v6
	v_lshl_add_u64 v[156:157], s[50:51], 0, v[4:5]
	v_mov_b32_e32 v243, v4
	v_lshl_add_u64 v[158:159], s[50:51], 0, v[2:3]
	v_mov_b32_e32 v244, v2
	s_add_u32 s94, s2, s50
	s_addc_u32 s95, s3, s51
	s_add_u32 s96, s2, s48
	s_addc_u32 s97, s3, s49
	v_add3_u32 v168, s63, v15, v168
	v_mov_b32_e32 v2, v149
	v_mov_b32_e32 v4, v149
	v_mov_b32_e32 v6, v149
	v_mov_b32_e32 v8, v149
	v_mov_b32_e32 v10, v149
	v_mov_b32_e32 v11, v149
	v_mov_b32_e32 v12, v149
	v_mov_b32_e32 v13, v149
	v_mov_b32_e32 v14, v149
	v_mov_b32_e32 v15, v149
	v_mov_b64_e32 v[32:33], v[16:17]
	v_mov_b64_e32 v[48:49], v[16:17]
	v_mov_b64_e32 v[64:65], v[16:17]
	v_cmp_gt_u32_e64 s[0:1], 32, v167
	v_mov_b32_e32 v173, 0
	v_mov_b32_e32 v206, 0
	v_mov_b32_e32 v207, 0
	v_mov_b32_e32 v208, 0
	v_mov_b32_e32 v209, 0
	v_mov_b32_e32 v210, 0
	v_mov_b32_e32 v211, 0
	v_mov_b32_e32 v212, 0
	v_mov_b32_e32 v213, 0
	v_mov_b32_e32 v214, 0
	v_mov_b32_e32 v215, 0
	v_mov_b32_e32 v216, 0
	v_mov_b32_e32 v217, 0
	v_mov_b32_e32 v218, 0
	v_mov_b32_e32 v219, 0
	v_mov_b32_e32 v220, 0
	v_mov_b32_e32 v221, 0
	v_mov_b64_e32 v[30:31], v[14:15]
	v_mov_b64_e32 v[28:29], v[12:13]
	v_mov_b64_e32 v[26:27], v[10:11]
	v_mov_b64_e32 v[24:25], v[8:9]
	v_mov_b64_e32 v[22:23], v[6:7]
	v_mov_b64_e32 v[20:21], v[4:5]
	v_mov_b64_e32 v[18:19], v[2:3]
	v_mov_b64_e32 v[46:47], v[14:15]
	v_mov_b64_e32 v[44:45], v[12:13]
	v_mov_b64_e32 v[42:43], v[10:11]
	v_mov_b64_e32 v[40:41], v[8:9]
	v_mov_b64_e32 v[38:39], v[6:7]
	v_mov_b64_e32 v[36:37], v[4:5]
	v_mov_b64_e32 v[34:35], v[2:3]
	v_mov_b64_e32 v[62:63], v[14:15]
	v_mov_b64_e32 v[60:61], v[12:13]
	v_mov_b64_e32 v[58:59], v[10:11]
	v_mov_b64_e32 v[56:57], v[8:9]
	v_mov_b64_e32 v[54:55], v[6:7]
	v_mov_b64_e32 v[52:53], v[4:5]
	v_mov_b64_e32 v[50:51], v[2:3]
	v_mov_b32_e32 v174, 0
	s_cmp_ge_u32 s64, 0x1000
	s_cbranch_scc0 .Lprio_skip_a1
	s_setprio 1

.LBB0_817:
	s_or_b64 exec, exec, s[56:57]
	s_waitcnt lgkmcnt(0)
	s_lshl_b64 s[0:1], s[54:55], 11
	s_add_u32 s0, s61, s0
	s_addc_u32 s1, s62, s1
	s_add_u32 s0, s0, s79
	s_addc_u32 s1, s1, 0
	s_mov_b32 s56, 0x05040100
	v_and_b32_e32 v85, 3, v164
	v_lshl_add_u32 v83, v85, 8, v85
	v_add_u32_e32 v83, 0x0c0c0400, v83
	v_lshrrev_b32_e32 v87, 5, v164
	v_lshl_add_u32 v84, v87, 2, v85
	v_lshlrev_b32_e32 v84, 11, v84
	v_and_b32_e32 v85, 28, v164
	v_add_u32_e32 v84, v84, v85
	v_lshl_add_u32 v87, v87, 4, s65
	ds_read_b128 v[66:69], v87 offset:128
	v_mov_b32_e32 v86, v84
	s_waitcnt lgkmcnt(0)
	v_mul_f32_e32 v66, 0x41800000, v66
	v_mul_f32_e32 v67, 0x41800000, v67
	v_mul_f32_e32 v68, 0x41800000, v68
	v_mul_f32_e32 v69, 0x41800000, v69
	v_mul_f32_e32 v70, v50, v66
	v_mul_f32_e32 v71, v51, v67
	v_mul_f32_e32 v72, v52, v68
	v_mul_f32_e32 v73, v53, v69
	v_med3_f32 v70, v70, s77, v166
	v_med3_f32 v71, v71, s77, v166
	v_med3_f32 v72, v72, s77, v166
	v_med3_f32 v73, v73, s77, v166
	v_cvt_pk_fp8_f32 v74, v70, v71
	v_cvt_pk_fp8_f32 v74, v72, v73 op_sel:[0,0,1]
	s_nop 1
	v_mov_b32_dpp v75, v74 quad_perm:[0,0,0,0] row_mask:0xf bank_mask:0xf
	v_mov_b32_dpp v76, v74 quad_perm:[1,1,1,1] row_mask:0xf bank_mask:0xf
	v_mov_b32_dpp v77, v74 quad_perm:[2,2,2,2] row_mask:0xf bank_mask:0xf
	v_mov_b32_dpp v78, v74 quad_perm:[3,3,3,3] row_mask:0xf bank_mask:0xf
	v_perm_b32 v80, v76, v75, v83
	v_perm_b32 v81, v78, v77, v83
	v_perm_b32 v82, v81, v80, s56
	global_store_dword v86, v82, s[0:1]
	v_mul_f32_e32 v70, v34, v66
	v_mul_f32_e32 v71, v35, v67
	v_mul_f32_e32 v72, v36, v68
	v_mul_f32_e32 v73, v37, v69
	v_med3_f32 v70, v70, s77, v166
	v_med3_f32 v71, v71, s77, v166
	v_med3_f32 v72, v72, s77, v166
	v_med3_f32 v73, v73, s77, v166
	v_cvt_pk_fp8_f32 v74, v70, v71
	v_cvt_pk_fp8_f32 v74, v72, v73 op_sel:[0,0,1]
	s_nop 1
	v_mov_b32_dpp v75, v74 quad_perm:[0,0,0,0] row_mask:0xf bank_mask:0xf
	v_mov_b32_dpp v76, v74 quad_perm:[1,1,1,1] row_mask:0xf bank_mask:0xf
	v_mov_b32_dpp v77, v74 quad_perm:[2,2,2,2] row_mask:0xf bank_mask:0xf
	v_mov_b32_dpp v78, v74 quad_perm:[3,3,3,3] row_mask:0xf bank_mask:0xf
	v_perm_b32 v80, v76, v75, v83
	v_perm_b32 v81, v78, v77, v83
	v_perm_b32 v82, v81, v80, s56
	global_store_dword v86, v82, s[0:1] offset:32
	v_mul_f32_e32 v70, v18, v66
	v_mul_f32_e32 v71, v19, v67
	v_mul_f32_e32 v72, v20, v68
	v_mul_f32_e32 v73, v21, v69
	v_med3_f32 v70, v70, s77, v166
	v_med3_f32 v71, v71, s77, v166
	v_med3_f32 v72, v72, s77, v166
	v_med3_f32 v73, v73, s77, v166
	v_cvt_pk_fp8_f32 v74, v70, v71
	v_cvt_pk_fp8_f32 v74, v72, v73 op_sel:[0,0,1]
	s_nop 1
	v_mov_b32_dpp v75, v74 quad_perm:[0,0,0,0] row_mask:0xf bank_mask:0xf
	v_mov_b32_dpp v76, v74 quad_perm:[1,1,1,1] row_mask:0xf bank_mask:0xf
	v_mov_b32_dpp v77, v74 quad_perm:[2,2,2,2] row_mask:0xf bank_mask:0xf
	v_mov_b32_dpp v78, v74 quad_perm:[3,3,3,3] row_mask:0xf bank_mask:0xf
	v_perm_b32 v80, v76, v75, v83
	v_perm_b32 v81, v78, v77, v83
	v_perm_b32 v82, v81, v80, s56
	global_store_dword v86, v82, s[0:1] offset:64
	v_mul_f32_e32 v70, v2, v66
	v_mul_f32_e32 v71, v3, v67
	v_mul_f32_e32 v72, v4, v68
	v_mul_f32_e32 v73, v5, v69
	v_med3_f32 v70, v70, s77, v166
	v_med3_f32 v71, v71, s77, v166
	v_med3_f32 v72, v72, s77, v166
	v_med3_f32 v73, v73, s77, v166
	v_cvt_pk_fp8_f32 v74, v70, v71
	v_cvt_pk_fp8_f32 v74, v72, v73 op_sel:[0,0,1]
	s_nop 1
	v_mov_b32_dpp v75, v74 quad_perm:[0,0,0,0] row_mask:0xf bank_mask:0xf
	v_mov_b32_dpp v76, v74 quad_perm:[1,1,1,1] row_mask:0xf bank_mask:0xf
	v_mov_b32_dpp v77, v74 quad_perm:[2,2,2,2] row_mask:0xf bank_mask:0xf
	v_mov_b32_dpp v78, v74 quad_perm:[3,3,3,3] row_mask:0xf bank_mask:0xf
	v_perm_b32 v80, v76, v75, v83
	v_perm_b32 v81, v78, v77, v83
	v_perm_b32 v82, v81, v80, s56
	global_store_dword v86, v82, s[0:1] offset:96
	ds_read_b128 v[66:69], v87 offset:160
	v_add_u32_e32 v86, 0x4000, v84
	s_waitcnt lgkmcnt(0)
	v_mul_f32_e32 v66, 0x41800000, v66
	v_mul_f32_e32 v67, 0x41800000, v67
	v_mul_f32_e32 v68, 0x41800000, v68
	v_mul_f32_e32 v69, 0x41800000, v69
	v_mul_f32_e32 v70, v54, v66
	v_mul_f32_e32 v71, v55, v67
	v_mul_f32_e32 v72, v56, v68
	v_mul_f32_e32 v73, v57, v69
	v_med3_f32 v70, v70, s77, v166
	v_med3_f32 v71, v71, s77, v166
	v_med3_f32 v72, v72, s77, v166
	v_med3_f32 v73, v73, s77, v166
	v_cvt_pk_fp8_f32 v74, v70, v71
	v_cvt_pk_fp8_f32 v74, v72, v73 op_sel:[0,0,1]
	s_nop 1
	v_mov_b32_dpp v75, v74 quad_perm:[0,0,0,0] row_mask:0xf bank_mask:0xf
	v_mov_b32_dpp v76, v74 quad_perm:[1,1,1,1] row_mask:0xf bank_mask:0xf
	v_mov_b32_dpp v77, v74 quad_perm:[2,2,2,2] row_mask:0xf bank_mask:0xf
	v_mov_b32_dpp v78, v74 quad_perm:[3,3,3,3] row_mask:0xf bank_mask:0xf
	v_perm_b32 v80, v76, v75, v83
	v_perm_b32 v81, v78, v77, v83
	v_perm_b32 v82, v81, v80, s56
	global_store_dword v86, v82, s[0:1]
	v_mul_f32_e32 v70, v38, v66
	v_mul_f32_e32 v71, v39, v67
	v_mul_f32_e32 v72, v40, v68
	v_mul_f32_e32 v73, v41, v69
	v_med3_f32 v70, v70, s77, v166
	v_med3_f32 v71, v71, s77, v166
	v_med3_f32 v72, v72, s77, v166
	v_med3_f32 v73, v73, s77, v166
	v_cvt_pk_fp8_f32 v74, v70, v71
	v_cvt_pk_fp8_f32 v74, v72, v73 op_sel:[0,0,1]
	s_nop 1
	v_mov_b32_dpp v75, v74 quad_perm:[0,0,0,0] row_mask:0xf bank_mask:0xf
	v_mov_b32_dpp v76, v74 quad_perm:[1,1,1,1] row_mask:0xf bank_mask:0xf
	v_mov_b32_dpp v77, v74 quad_perm:[2,2,2,2] row_mask:0xf bank_mask:0xf
	v_mov_b32_dpp v78, v74 quad_perm:[3,3,3,3] row_mask:0xf bank_mask:0xf
	v_perm_b32 v80, v76, v75, v83
	v_perm_b32 v81, v78, v77, v83
	v_perm_b32 v82, v81, v80, s56
	global_store_dword v86, v82, s[0:1] offset:32
	v_mul_f32_e32 v70, v22, v66
	v_mul_f32_e32 v71, v23, v67
	v_mul_f32_e32 v72, v24, v68
	v_mul_f32_e32 v73, v25, v69
	v_med3_f32 v70, v70, s77, v166
	v_med3_f32 v71, v71, s77, v166
	v_med3_f32 v72, v72, s77, v166
	v_med3_f32 v73, v73, s77, v166
	v_cvt_pk_fp8_f32 v74, v70, v71
	v_cvt_pk_fp8_f32 v74, v72, v73 op_sel:[0,0,1]
	s_nop 1
	v_mov_b32_dpp v75, v74 quad_perm:[0,0,0,0] row_mask:0xf bank_mask:0xf
	v_mov_b32_dpp v76, v74 quad_perm:[1,1,1,1] row_mask:0xf bank_mask:0xf
	v_mov_b32_dpp v77, v74 quad_perm:[2,2,2,2] row_mask:0xf bank_mask:0xf
	v_mov_b32_dpp v78, v74 quad_perm:[3,3,3,3] row_mask:0xf bank_mask:0xf
	v_perm_b32 v80, v76, v75, v83
	v_perm_b32 v81, v78, v77, v83
	v_perm_b32 v82, v81, v80, s56
	global_store_dword v86, v82, s[0:1] offset:64
	v_mul_f32_e32 v70, v6, v66
	v_mul_f32_e32 v71, v7, v67
	v_mul_f32_e32 v72, v8, v68
	v_mul_f32_e32 v73, v9, v69
	v_med3_f32 v70, v70, s77, v166
	v_med3_f32 v71, v71, s77, v166
	v_med3_f32 v72, v72, s77, v166
	v_med3_f32 v73, v73, s77, v166
	v_cvt_pk_fp8_f32 v74, v70, v71
	v_cvt_pk_fp8_f32 v74, v72, v73 op_sel:[0,0,1]
	s_nop 1
	v_mov_b32_dpp v75, v74 quad_perm:[0,0,0,0] row_mask:0xf bank_mask:0xf
	v_mov_b32_dpp v76, v74 quad_perm:[1,1,1,1] row_mask:0xf bank_mask:0xf
	v_mov_b32_dpp v77, v74 quad_perm:[2,2,2,2] row_mask:0xf bank_mask:0xf
	v_mov_b32_dpp v78, v74 quad_perm:[3,3,3,3] row_mask:0xf bank_mask:0xf
	v_perm_b32 v80, v76, v75, v83
	v_perm_b32 v81, v78, v77, v83
	v_perm_b32 v82, v81, v80, s56
	global_store_dword v86, v82, s[0:1] offset:96
	ds_read_b128 v[66:69], v87 offset:192
	v_add_u32_e32 v86, 0x8000, v84
	s_waitcnt lgkmcnt(0)
	v_mul_f32_e32 v66, 0x41800000, v66
	v_mul_f32_e32 v67, 0x41800000, v67
	v_mul_f32_e32 v68, 0x41800000, v68
	v_mul_f32_e32 v69, 0x41800000, v69
	v_mul_f32_e32 v70, v58, v66
	v_mul_f32_e32 v71, v59, v67
	v_mul_f32_e32 v72, v60, v68
	v_mul_f32_e32 v73, v61, v69
	v_med3_f32 v70, v70, s77, v166
	v_med3_f32 v71, v71, s77, v166
	v_med3_f32 v72, v72, s77, v166
	v_med3_f32 v73, v73, s77, v166
	v_cvt_pk_fp8_f32 v74, v70, v71
	v_cvt_pk_fp8_f32 v74, v72, v73 op_sel:[0,0,1]
	s_nop 1
	v_mov_b32_dpp v75, v74 quad_perm:[0,0,0,0] row_mask:0xf bank_mask:0xf
	v_mov_b32_dpp v76, v74 quad_perm:[1,1,1,1] row_mask:0xf bank_mask:0xf
	v_mov_b32_dpp v77, v74 quad_perm:[2,2,2,2] row_mask:0xf bank_mask:0xf
	v_mov_b32_dpp v78, v74 quad_perm:[3,3,3,3] row_mask:0xf bank_mask:0xf
	v_perm_b32 v80, v76, v75, v83
	v_perm_b32 v81, v78, v77, v83
	v_perm_b32 v82, v81, v80, s56
	global_store_dword v86, v82, s[0:1]
	v_mul_f32_e32 v70, v42, v66
	v_mul_f32_e32 v71, v43, v67
	v_mul_f32_e32 v72, v44, v68
	v_mul_f32_e32 v73, v45, v69
	v_med3_f32 v70, v70, s77, v166
	v_med3_f32 v71, v71, s77, v166
	v_med3_f32 v72, v72, s77, v166
	v_med3_f32 v73, v73, s77, v166
	v_cvt_pk_fp8_f32 v74, v70, v71
	v_cvt_pk_fp8_f32 v74, v72, v73 op_sel:[0,0,1]
	s_nop 1
	v_mov_b32_dpp v75, v74 quad_perm:[0,0,0,0] row_mask:0xf bank_mask:0xf
	v_mov_b32_dpp v76, v74 quad_perm:[1,1,1,1] row_mask:0xf bank_mask:0xf
	v_mov_b32_dpp v77, v74 quad_perm:[2,2,2,2] row_mask:0xf bank_mask:0xf
	v_mov_b32_dpp v78, v74 quad_perm:[3,3,3,3] row_mask:0xf bank_mask:0xf
	v_perm_b32 v80, v76, v75, v83
	v_perm_b32 v81, v78, v77, v83
	v_perm_b32 v82, v81, v80, s56
	global_store_dword v86, v82, s[0:1] offset:32
	v_mul_f32_e32 v70, v26, v66
	v_mul_f32_e32 v71, v27, v67
	v_mul_f32_e32 v72, v28, v68
	v_mul_f32_e32 v73, v29, v69
	v_med3_f32 v70, v70, s77, v166
	v_med3_f32 v71, v71, s77, v166
	v_med3_f32 v72, v72, s77, v166
	v_med3_f32 v73, v73, s77, v166
	v_cvt_pk_fp8_f32 v74, v70, v71
	v_cvt_pk_fp8_f32 v74, v72, v73 op_sel:[0,0,1]
	s_nop 1
	v_mov_b32_dpp v75, v74 quad_perm:[0,0,0,0] row_mask:0xf bank_mask:0xf
	v_mov_b32_dpp v76, v74 quad_perm:[1,1,1,1] row_mask:0xf bank_mask:0xf
	v_mov_b32_dpp v77, v74 quad_perm:[2,2,2,2] row_mask:0xf bank_mask:0xf
	v_mov_b32_dpp v78, v74 quad_perm:[3,3,3,3] row_mask:0xf bank_mask:0xf
	v_perm_b32 v80, v76, v75, v83
	v_perm_b32 v81, v78, v77, v83
	v_perm_b32 v82, v81, v80, s56
	global_store_dword v86, v82, s[0:1] offset:64
	v_mul_f32_e32 v70, v10, v66
	v_mul_f32_e32 v71, v11, v67
	v_mul_f32_e32 v72, v12, v68
	v_mul_f32_e32 v73, v13, v69
	v_med3_f32 v70, v70, s77, v166
	v_med3_f32 v71, v71, s77, v166
	v_med3_f32 v72, v72, s77, v166
	v_med3_f32 v73, v73, s77, v166
	v_cvt_pk_fp8_f32 v74, v70, v71
	v_cvt_pk_fp8_f32 v74, v72, v73 op_sel:[0,0,1]
	s_nop 1
	v_mov_b32_dpp v75, v74 quad_perm:[0,0,0,0] row_mask:0xf bank_mask:0xf
	v_mov_b32_dpp v76, v74 quad_perm:[1,1,1,1] row_mask:0xf bank_mask:0xf
	v_mov_b32_dpp v77, v74 quad_perm:[2,2,2,2] row_mask:0xf bank_mask:0xf
	v_mov_b32_dpp v78, v74 quad_perm:[3,3,3,3] row_mask:0xf bank_mask:0xf
	v_perm_b32 v80, v76, v75, v83
	v_perm_b32 v81, v78, v77, v83
	v_perm_b32 v82, v81, v80, s56
	global_store_dword v86, v82, s[0:1] offset:96
	ds_read_b128 v[66:69], v87 offset:224
	v_add_u32_e32 v86, 0xc000, v84
	s_waitcnt lgkmcnt(0)
	v_mul_f32_e32 v66, 0x41800000, v66
	v_mul_f32_e32 v67, 0x41800000, v67
	v_mul_f32_e32 v68, 0x41800000, v68
	v_mul_f32_e32 v69, 0x41800000, v69
	v_mul_f32_e32 v70, v62, v66
	v_mul_f32_e32 v71, v63, v67
	v_mul_f32_e32 v72, v64, v68
	v_mul_f32_e32 v73, v65, v69
	v_med3_f32 v70, v70, s77, v166
	v_med3_f32 v71, v71, s77, v166
	v_med3_f32 v72, v72, s77, v166
	v_med3_f32 v73, v73, s77, v166
	v_cvt_pk_fp8_f32 v74, v70, v71
	v_cvt_pk_fp8_f32 v74, v72, v73 op_sel:[0,0,1]
	s_nop 1
	v_mov_b32_dpp v75, v74 quad_perm:[0,0,0,0] row_mask:0xf bank_mask:0xf
	v_mov_b32_dpp v76, v74 quad_perm:[1,1,1,1] row_mask:0xf bank_mask:0xf
	v_mov_b32_dpp v77, v74 quad_perm:[2,2,2,2] row_mask:0xf bank_mask:0xf
	v_mov_b32_dpp v78, v74 quad_perm:[3,3,3,3] row_mask:0xf bank_mask:0xf
	v_perm_b32 v80, v76, v75, v83
	v_perm_b32 v81, v78, v77, v83
	v_perm_b32 v82, v81, v80, s56
	global_store_dword v86, v82, s[0:1]
	v_mul_f32_e32 v70, v46, v66
	v_mul_f32_e32 v71, v47, v67
	v_mul_f32_e32 v72, v48, v68
	v_mul_f32_e32 v73, v49, v69
	v_med3_f32 v70, v70, s77, v166
	v_med3_f32 v71, v71, s77, v166
	v_med3_f32 v72, v72, s77, v166
	v_med3_f32 v73, v73, s77, v166
	v_cvt_pk_fp8_f32 v74, v70, v71
	v_cvt_pk_fp8_f32 v74, v72, v73 op_sel:[0,0,1]
	s_nop 1
	v_mov_b32_dpp v75, v74 quad_perm:[0,0,0,0] row_mask:0xf bank_mask:0xf
	v_mov_b32_dpp v76, v74 quad_perm:[1,1,1,1] row_mask:0xf bank_mask:0xf
	v_mov_b32_dpp v77, v74 quad_perm:[2,2,2,2] row_mask:0xf bank_mask:0xf
	v_mov_b32_dpp v78, v74 quad_perm:[3,3,3,3] row_mask:0xf bank_mask:0xf
	v_perm_b32 v80, v76, v75, v83
	v_perm_b32 v81, v78, v77, v83
	v_perm_b32 v82, v81, v80, s56
	global_store_dword v86, v82, s[0:1] offset:32
	v_mul_f32_e32 v70, v30, v66
	v_mul_f32_e32 v71, v31, v67
	v_mul_f32_e32 v72, v32, v68
	v_mul_f32_e32 v73, v33, v69
	v_med3_f32 v70, v70, s77, v166
	v_med3_f32 v71, v71, s77, v166
	v_med3_f32 v72, v72, s77, v166
	v_med3_f32 v73, v73, s77, v166
	v_cvt_pk_fp8_f32 v74, v70, v71
	v_cvt_pk_fp8_f32 v74, v72, v73 op_sel:[0,0,1]
	s_nop 1
	v_mov_b32_dpp v75, v74 quad_perm:[0,0,0,0] row_mask:0xf bank_mask:0xf
	v_mov_b32_dpp v76, v74 quad_perm:[1,1,1,1] row_mask:0xf bank_mask:0xf
	v_mov_b32_dpp v77, v74 quad_perm:[2,2,2,2] row_mask:0xf bank_mask:0xf
	v_mov_b32_dpp v78, v74 quad_perm:[3,3,3,3] row_mask:0xf bank_mask:0xf
	v_perm_b32 v80, v76, v75, v83
	v_perm_b32 v81, v78, v77, v83
	v_perm_b32 v82, v81, v80, s56
	global_store_dword v86, v82, s[0:1] offset:64
	v_mul_f32_e32 v70, v14, v66
	v_mul_f32_e32 v71, v15, v67
	v_mul_f32_e32 v72, v16, v68
	v_mul_f32_e32 v73, v17, v69
	v_med3_f32 v70, v70, s77, v166
	v_med3_f32 v71, v71, s77, v166
	v_med3_f32 v72, v72, s77, v166
	v_med3_f32 v73, v73, s77, v166
	v_cvt_pk_fp8_f32 v74, v70, v71
	v_cvt_pk_fp8_f32 v74, v72, v73 op_sel:[0,0,1]
	s_nop 1
	v_mov_b32_dpp v75, v74 quad_perm:[0,0,0,0] row_mask:0xf bank_mask:0xf
	v_mov_b32_dpp v76, v74 quad_perm:[1,1,1,1] row_mask:0xf bank_mask:0xf
	v_mov_b32_dpp v77, v74 quad_perm:[2,2,2,2] row_mask:0xf bank_mask:0xf
	v_mov_b32_dpp v78, v74 quad_perm:[3,3,3,3] row_mask:0xf bank_mask:0xf
	v_perm_b32 v80, v76, v75, v83
	v_perm_b32 v81, v78, v77, v83
	v_perm_b32 v82, v81, v80, s56
	global_store_dword v86, v82, s[0:1] offset:96


	s_lshl_b32 s55, s80, 8
	s_and_b32 s0, s81, 15
	s_add_i32 s55, s55, s63
	s_lshl_b32 s54, s0, 8
	v_mov_b32_e32 v168, v1
	s_ashr_i32 s0, s55, 31
	s_add_u32 s52, s52, s55
	v_and_b32_e32 v167, 31, v168
	v_or_b32_e32 v30, s52, v167
	v_mov_b64_e32 v[2:3], s[6:7]
	s_addc_u32 s53, s53, s0
	v_mad_u64_u32 v[2:3], s[0:1], v30, s68, v[2:3]
	v_bfe_u32 v169, v168, 5, 1
	v_mad_i32_i24 v3, s53, v162, v3
	s_lshl_b32 s12, s82, 1
	v_lshl_add_u64 v[2:3], v[2:3], 0, s[12:13]
	v_lshlrev_b32_e32 v148, 4, v169
	v_lshl_add_u64 v[44:45], v[2:3], 0, v[148:149]
	global_load_dwordx4 v[32:35], v[44:45], off
	global_load_dwordx4 v[36:39], v[44:45], off offset:32
	global_load_dwordx4 v[26:29], v[44:45], off offset:64
	global_load_dwordx4 v[22:25], v[44:45], off offset:96
	global_load_dwordx4 v[18:21], v[44:45], off offset:128
	global_load_dwordx4 v[14:17], v[44:45], off offset:160
	global_load_dwordx4 v[10:13], v[44:45], off offset:192
	v_and_b32_e32 v118, 32, v168
	global_load_dwordx4 v[6:9], v118, s[4:5] offset:576
	s_waitcnt lgkmcnt(0)
	global_load_dwordx4 v[2:5], v118, s[4:5] offset:592
	global_load_dwordx4 v[102:105], v118, s[4:5] offset:704
	global_load_dwordx4 v[110:113], v118, s[4:5] offset:720
	global_load_dwordx4 v[40:43], v[44:45], off offset:224
	global_load_dwordx4 v[82:85], v[44:45], off offset:256
	global_load_dwordx4 v[138:141], v[44:45], off offset:288
	global_load_dwordx4 v[70:73], v[44:45], off offset:320
	global_load_dwordx4 v[142:145], v[44:45], off offset:352
	v_mov_b32_e32 v31, s53
	s_mov_b32 m0, s71
	s_mov_b32 s12, 1
	v_mul_hi_i32 v150, v168, s70
	v_lshrrev_b32_e32 v151, 31, v150
	v_ashrrev_i32_e32 v150, 2, v150
	v_add_u32_e32 v150, v150, v151
	v_mul_lo_u32 v151, v150, 24
	v_sub_u32_e32 v151, v168, v151
	v_lshrrev_b32_e32 v152, 1, v150
	v_bitop3_b32 v151, v152, v151, 7 bitop3:0x6c
	v_mul_lo_u32 v150, v150, s68
	v_lshl_add_u32 v150, v151, 4, v150
	v_add_u32_e32 v151, 0x200, v168
	v_mul_hi_i32 v153, v151, s70
	v_lshrrev_b32_e32 v154, 31, v153
	v_ashrrev_i32_e32 v153, 2, v153
	v_add_u32_e32 v153, v153, v154
	v_mul_lo_u32 v154, v153, 24
	v_sub_u32_e32 v154, v151, v154
	v_lshrrev_b32_e32 v152, 1, v153
	v_bitop3_b32 v154, v152, v154, 7 bitop3:0x6c
	v_mul_lo_u32 v153, v153, s68
	v_lshl_add_u32 v153, v154, 4, v153
	v_add_u32_e32 v154, 0x400, v168
	v_mul_hi_i32 v155, v154, s70
	v_lshrrev_b32_e32 v156, 31, v155
	v_ashrrev_i32_e32 v155, 2, v155
	v_add_u32_e32 v155, v155, v156
	v_mul_lo_u32 v156, v155, 24
	v_sub_u32_e32 v154, v154, v156
	v_lshrrev_b32_e32 v152, 1, v155
	v_bitop3_b32 v154, v152, v154, 7 bitop3:0x6c
	v_mul_lo_u32 v155, v155, s68
	v_ashrrev_i32_e32 v157, 4, v168
	v_lshl_add_u32 v155, v154, 4, v155
	v_bfe_u32 v154, v168, 2, 2
	v_lshrrev_b32_e32 v156, 1, v168
	v_and_b32_e32 v158, 0x1ffff0, v157
	v_lshrrev_b32_e32 v157, 1, v157
	v_ashrrev_i32_e32 v151, 4, v151
	v_and_or_b32 v154, v156, 8, v154
	v_and_b32_e32 v156, 0x60, v168
	v_lshlrev_b32_e32 v159, 3, v168
	v_and_b32_e32 v157, 4, v157
	v_and_b32_e32 v170, 0x1ffff0, v151
	v_lshrrev_b32_e32 v151, 1, v151
	v_and_or_b32 v156, v159, 24, v156
	v_or3_b32 v157, v158, v157, v154
	v_and_b32_e32 v151, 4, v151
	s_barrier
	global_load_lds_dwordx4 v150, s[44:45]
	s_mov_b32 m0, s72
	v_lshlrev_b32_e32 v156, 1, v156
	v_lshlrev_b32_e32 v158, 11, v157
	v_or3_b32 v151, v170, v151, v154
	global_load_lds_dwordx4 v153, s[44:45]
	s_mov_b32 m0, s73
	v_or_b32_e32 v157, v158, v156
	v_lshlrev_b32_e32 v170, 11, v151
	global_load_lds_dwordx4 v155, s[44:45]
	s_mov_b32 m0, s64
	v_or_b32_e32 v151, v170, v156
	global_load_lds_dwordx4 v157, s[46:47]
	s_mov_b32 m0, s74
	v_lshlrev_b32_e32 v171, 1, v168
	global_load_lds_dwordx4 v151, s[46:47]
	s_waitcnt vmcnt(0)
	v_and_b32_e32 v191, 0xffff0000, v32
	v_lshlrev_b32_e32 v190, 16, v32
	v_lshlrev_b32_e32 v206, 16, v26
	v_and_b32_e32 v207, 0xffff0000, v26
	v_lshlrev_b32_e32 v208, 16, v27
	v_and_b32_e32 v209, 0xffff0000, v27
	v_lshlrev_b32_e32 v210, 16, v28
	v_and_b32_e32 v211, 0xffff0000, v28
	v_lshlrev_b32_e32 v212, 16, v29
	v_and_b32_e32 v213, 0xffff0000, v29
	v_lshlrev_b32_e32 v222, 16, v18
	v_and_b32_e32 v223, 0xffff0000, v18
	v_lshlrev_b32_e32 v224, 16, v19
	v_and_b32_e32 v225, 0xffff0000, v19
	v_lshlrev_b32_e32 v226, 16, v20
	v_and_b32_e32 v227, 0xffff0000, v20
	v_lshlrev_b32_e32 v228, 16, v21
	v_and_b32_e32 v229, 0xffff0000, v21
	global_load_dwordx4 v[26:29], v118, s[4:5] offset:640
	global_load_dwordx4 v[156:159], v118, s[4:5] offset:656
	global_load_dwordx4 v[18:21], v118, s[4:5] offset:528
	v_mul_f32_e32 v188, v191, v191
	v_lshlrev_b32_e32 v192, 16, v33
	v_fmac_f32_e32 v188, v190, v190
	v_and_b32_e32 v193, 0xffff0000, v33
	v_fmac_f32_e32 v188, v192, v192
	v_lshlrev_b32_e32 v194, 16, v34
	v_fmac_f32_e32 v188, v193, v193
	v_and_b32_e32 v195, 0xffff0000, v34
	v_fmac_f32_e32 v188, v194, v194
	v_lshlrev_b32_e32 v196, 16, v35
	v_fmac_f32_e32 v188, v195, v195
	v_and_b32_e32 v197, 0xffff0000, v35
	v_fmac_f32_e32 v188, v196, v196
	v_lshlrev_b32_e32 v198, 16, v36
	v_fmac_f32_e32 v188, v197, v197
	v_and_b32_e32 v199, 0xffff0000, v36
	v_fmac_f32_e32 v188, v198, v198
	v_lshlrev_b32_e32 v200, 16, v37
	v_lshlrev_b32_e32 v214, 16, v22
	v_and_b32_e32 v215, 0xffff0000, v22
	v_lshlrev_b32_e32 v216, 16, v23
	v_and_b32_e32 v217, 0xffff0000, v23
	v_lshlrev_b32_e32 v218, 16, v24
	v_and_b32_e32 v219, 0xffff0000, v24
	v_lshlrev_b32_e32 v220, 16, v25
	v_and_b32_e32 v221, 0xffff0000, v25
	v_fmac_f32_e32 v188, v199, v199
	global_load_dwordx4 v[22:25], v118, s[4:5] offset:512
	v_and_b32_e32 v201, 0xffff0000, v37
	v_fmac_f32_e32 v188, v200, v200
	v_lshlrev_b32_e32 v202, 16, v38
	v_fmac_f32_e32 v188, v201, v201
	v_and_b32_e32 v203, 0xffff0000, v38
	v_fmac_f32_e32 v188, v202, v202
	v_lshlrev_b32_e32 v204, 16, v39
	v_fmac_f32_e32 v188, v203, v203
	v_and_b32_e32 v205, 0xffff0000, v39
	v_fmac_f32_e32 v188, v204, v204
	v_fmac_f32_e32 v188, v205, v205
	v_fmac_f32_e32 v188, v206, v206
	v_fmac_f32_e32 v188, v207, v207
	v_fmac_f32_e32 v188, v208, v208
	v_fmac_f32_e32 v188, v209, v209
	v_fmac_f32_e32 v188, v210, v210
	v_fmac_f32_e32 v188, v211, v211
	v_fmac_f32_e32 v188, v212, v212
	v_fmac_f32_e32 v188, v213, v213
	v_fmac_f32_e32 v188, v214, v214
	v_fmac_f32_e32 v188, v215, v215
	v_fmac_f32_e32 v188, v216, v216
	v_fmac_f32_e32 v188, v217, v217
	v_fmac_f32_e32 v188, v218, v218
	v_fmac_f32_e32 v188, v219, v219
	v_fmac_f32_e32 v188, v220, v220
	v_fmac_f32_e32 v188, v221, v221
	v_fmac_f32_e32 v188, v222, v222
	v_fmac_f32_e32 v188, v223, v223
	v_fmac_f32_e32 v188, v224, v224
	v_fmac_f32_e32 v188, v225, v225
	v_fmac_f32_e32 v188, v226, v226
	v_fmac_f32_e32 v188, v227, v227
	v_fmac_f32_e32 v188, v228, v228
	v_lshlrev_b32_e32 v230, 16, v14
	v_fmac_f32_e32 v188, v229, v229
	v_and_b32_e32 v231, 0xffff0000, v14
	v_fmac_f32_e32 v188, v230, v230
	v_lshlrev_b32_e32 v232, 16, v15
	v_fmac_f32_e32 v188, v231, v231
	v_and_b32_e32 v233, 0xffff0000, v15
	v_fmac_f32_e32 v188, v232, v232
	v_lshlrev_b32_e32 v234, 16, v16
	v_fmac_f32_e32 v188, v233, v233
	v_and_b32_e32 v235, 0xffff0000, v16
	v_fmac_f32_e32 v188, v234, v234
	v_lshlrev_b32_e32 v246, 16, v40
	v_and_b32_e32 v247, 0xffff0000, v40
	v_lshlrev_b32_e32 v248, 16, v41
	v_and_b32_e32 v249, 0xffff0000, v41
	v_lshlrev_b32_e32 v250, 16, v42
	v_and_b32_e32 v251, 0xffff0000, v42
	v_lshlrev_b32_e32 v252, 16, v43
	v_and_b32_e32 v253, 0xffff0000, v43
	global_load_dwordx4 v[106:109], v118, s[4:5] offset:16
	global_load_dwordx4 v[114:117], v118, s[4:5]
	global_load_dwordx4 v[94:97], v118, s[4:5] offset:80
	global_load_dwordx4 v[98:101], v118, s[4:5] offset:64
	global_load_dwordx4 v[86:89], v118, s[4:5] offset:144
	global_load_dwordx4 v[90:93], v118, s[4:5] offset:128
	global_load_dwordx4 v[74:77], v118, s[4:5] offset:208
	global_load_dwordx4 v[78:81], v118, s[4:5] offset:192
	global_load_dwordx4 v[62:65], v118, s[4:5] offset:272
	global_load_dwordx4 v[66:69], v118, s[4:5] offset:256
	global_load_dwordx4 v[54:57], v118, s[4:5] offset:336
	global_load_dwordx4 v[58:61], v118, s[4:5] offset:320
	global_load_dwordx4 v[46:49], v118, s[4:5] offset:400
	global_load_dwordx4 v[50:53], v118, s[4:5] offset:384
	global_load_dwordx4 v[38:41], v118, s[4:5] offset:464
	global_load_dwordx4 v[42:45], v118, s[4:5] offset:448
	v_lshlrev_b32_e32 v236, 16, v17
	v_fmac_f32_e32 v188, v235, v235
	v_and_b32_e32 v237, 0xffff0000, v17
	v_fmac_f32_e32 v188, v236, v236
	v_lshlrev_b32_e32 v238, 16, v10
	v_fmac_f32_e32 v188, v237, v237
	v_and_b32_e32 v239, 0xffff0000, v10
	v_fmac_f32_e32 v188, v238, v238
	v_lshlrev_b32_e32 v240, 16, v11
	v_fmac_f32_e32 v188, v239, v239
	v_and_b32_e32 v241, 0xffff0000, v11
	v_fmac_f32_e32 v188, v240, v240
	v_lshlrev_b32_e32 v242, 16, v12
	v_fmac_f32_e32 v188, v241, v241
	v_and_b32_e32 v243, 0xffff0000, v12
	v_fmac_f32_e32 v188, v242, v242
	v_lshlrev_b32_e32 v244, 16, v13
	v_fmac_f32_e32 v188, v243, v243
	v_and_b32_e32 v245, 0xffff0000, v13
	v_fmac_f32_e32 v188, v244, v244
	v_fmac_f32_e32 v188, v245, v245
	v_fmac_f32_e32 v188, v246, v246
	v_fmac_f32_e32 v188, v247, v247
	v_fmac_f32_e32 v188, v248, v248
	v_fmac_f32_e32 v188, v249, v249
	v_fmac_f32_e32 v188, v250, v250
	v_fmac_f32_e32 v188, v251, v251
	v_fmac_f32_e32 v188, v252, v252
	v_lshlrev_b32_e32 v187, 16, v82
	v_lshlrev_b32_e32 v186, 16, v70
	v_fmac_f32_e32 v188, v253, v253
	v_lshlrev_b32_e32 v124, 16, v144
	v_and_b32_e32 v126, 0xffff0000, v144
	v_lshlrev_b32_e32 v131, 16, v139
	v_and_b32_e32 v133, 0xffff0000, v139
	v_lshlrev_b32_e32 v137, 16, v138
	v_lshlrev_b32_e32 v136, 16, v142
	v_and_b32_e32 v139, 0xffff0000, v138
	v_and_b32_e32 v138, 0xffff0000, v142
	v_lshlrev_b32_e32 v142, 16, v73
	v_and_b32_e32 v144, 0xffff0000, v73
	v_lshlrev_b32_e32 v152, 16, v72
	v_and_b32_e32 v154, 0xffff0000, v72
	v_mul_f32_e32 v72, v186, v186
	v_mul_f32_e32 v73, v187, v187
	s_waitcnt vmcnt(18)
	v_mov_b32_e32 v150, v158
	v_mov_b32_e32 v158, v156
	v_lshlrev_b32_e32 v156, 16, v71
	v_and_b32_e32 v184, 0xffff0000, v71
	v_and_b32_e32 v189, 0xffff0000, v82
	v_add_f32_e32 v71, v73, v188
	v_and_b32_e32 v188, 0xffff0000, v70
	v_mov_b32_e32 v128, v110
	v_mov_b32_e32 v129, v2
	v_mov_b32_e32 v2, v111
	s_waitcnt vmcnt(17)
	v_mov_b32_e32 v151, v20
	v_mov_b32_e32 v20, v159
	v_mov_b32_e32 v159, v18
	v_mov_b32_e32 v18, v157
	v_lshlrev_b32_e32 v157, 16, v83
	v_mul_f32_e32 v110, v188, v188
	v_mul_f32_e32 v111, v189, v189
	v_lshlrev_b32_e32 v119, 16, v141
	v_and_b32_e32 v121, 0xffff0000, v141
	v_lshlrev_b32_e32 v125, 16, v140
	v_and_b32_e32 v127, 0xffff0000, v140
	v_mov_b32_e32 v140, v102
	v_mov_b32_e32 v141, v6
	v_mov_b32_e32 v6, v103
	v_mul_f32_e32 v102, v156, v156
	v_mul_f32_e32 v103, v157, v157
	v_and_b32_e32 v185, 0xffff0000, v83
	v_add_f32_e32 v70, v111, v71
	v_mov_b32_e32 v134, v104
	v_mov_b32_e32 v135, v8
	v_mov_b32_e32 v8, v105
	v_lshlrev_b32_e32 v153, 16, v84
	v_mul_f32_e32 v104, v184, v184
	v_mul_f32_e32 v105, v185, v185
	v_add_f32_e32 v70, v103, v70
	v_mul_f32_e32 v180, v152, v152
	v_mul_f32_e32 v181, v153, v153
	v_and_b32_e32 v155, 0xffff0000, v84
	v_add_f32_e32 v70, v105, v70
	v_lshlrev_b32_e32 v130, 16, v143
	v_and_b32_e32 v132, 0xffff0000, v143
	v_lshlrev_b32_e32 v143, 16, v85
	v_mul_f32_e32 v182, v154, v154
	v_mul_f32_e32 v183, v155, v155
	v_add_f32_e32 v70, v181, v70
	v_lshlrev_b32_e32 v118, 16, v145
	v_and_b32_e32 v120, 0xffff0000, v145
	v_mul_f32_e32 v176, v142, v142
	v_mul_f32_e32 v177, v143, v143
	v_and_b32_e32 v145, 0xffff0000, v85
	v_add_f32_e32 v70, v183, v70
	v_mul_f32_e32 v178, v144, v144
	v_mul_f32_e32 v179, v145, v145
	v_add_f32_e32 v70, v177, v70
	v_mul_f32_e32 v172, v136, v136
	v_mul_f32_e32 v173, v137, v137
	v_add_f32_e32 v70, v179, v70
	v_mul_f32_e32 v174, v138, v138
	v_mul_f32_e32 v175, v139, v139
	v_add_f32_e32 v70, v173, v70
	v_add_f32_e32 v70, v175, v70
	v_fmac_f32_e32 v70, v131, v131
	v_fmac_f32_e32 v70, v133, v133
	v_fmac_f32_e32 v70, v125, v125
	v_fmac_f32_e32 v70, v127, v127
	v_fmac_f32_e32 v70, v119, v119
	v_fmac_f32_e32 v70, v121, v121
	v_add_f32_e32 v103, v72, v70
	v_add_f32_e32 v103, v110, v103
	v_add_f32_e32 v102, v102, v103
	v_add_f32_e32 v173, v104, v102
	v_add_f32_e32 v173, v180, v173
	v_add_f32_e32 v173, v182, v173
	v_add_f32_e32 v173, v176, v173
	v_add_f32_e32 v173, v178, v173
	v_mov_b32_e32 v176, v132
	v_mov_b32_e32 v177, v130
	s_waitcnt vmcnt(16)
	v_mov_b32_e32 v179, v24
	v_add_f32_e32 v24, v172, v173
	v_lshlrev_b64 v[10:11], 8, v[30:31]
	v_mul_f32_e32 v176, v176, v176
	v_mul_f32_e32 v177, v177, v177
	v_add_f32_e32 v24, v174, v24
	v_lshl_add_u64 v[10:11], s[10:11], 0, v[10:11]
	v_lshlrev_b32_e32 v12, 6, v169
	v_mov_b32_e32 v13, v149
	v_mov_b32_e32 v180, v126
	v_mov_b32_e32 v181, v124
	v_add_f32_e32 v24, v177, v24
	v_lshl_add_u64 v[170:171], v[10:11], 0, v[12:13]
	v_mul_f32_e32 v180, v180, v180
	v_mul_f32_e32 v181, v181, v181
	v_add_f32_e32 v24, v176, v24
	global_load_dwordx4 v[10:13], v[170:171], off offset:48
	global_load_dwordx4 v[14:17], v[170:171], off offset:32
	global_load_dwordx4 v[30:33], v[170:171], off offset:16
	global_load_dwordx4 v[34:37], v[170:171], off
	v_mov_b32_e32 v122, v112
	v_mov_b32_e32 v123, v4
	v_mov_b32_e32 v4, v113
	global_load_dwordx4 v[70:73], v[170:171], off offset:176
	global_load_dwordx4 v[82:85], v[170:171], off offset:160
	global_load_dwordx4 v[102:105], v[170:171], off offset:144
	global_load_dwordx4 v[110:113], v[170:171], off offset:128
	v_mov_b32_e32 v170, v120
	v_mov_b32_e32 v171, v118
	v_add_f32_e32 v24, v181, v24
	v_mul_f32_e32 v170, v170, v170
	v_mul_f32_e32 v171, v171, v171
	v_add_f32_e32 v24, v180, v24
	v_add_f32_e32 v24, v171, v24
	v_add_f32_e32 v24, v170, v24
	v_mov_b32_e32 v178, v28
	v_mov_b32_e32 v28, v24
	s_nop 1
	v_permlane32_swap_b32_e32 v24, v28
	v_add_f32_e32 v24, v24, v28
	v_fmamk_f32 v24, v24, 0x3baaaaab, v163
	v_mul_f32_e32 v28, 0x4b800000, v24
	v_cmp_gt_f32_e32 vcc, s69, v24
	s_nop 1
	v_cndmask_b32_e32 v24, v24, v28, vcc
	v_rsq_f32_e32 v170, v24
	v_mov_b32_e32 v24, v29
	v_mov_b32_e32 v29, v22
	v_mov_b32_e32 v28, v26
	v_mul_f32_e32 v22, 0x45800000, v170
	v_cndmask_b32_e32 v22, v170, v22, vcc
	v_mul_f32_e32 v26, 0x3dd53b94, v22
	s_waitcnt vmcnt(22)
	v_mul_f32_e32 v22, v114, v26
	v_mul_f32_e32 v114, v22, v190
	v_mul_f32_e32 v22, v106, v26
	v_mul_f32_e32 v106, v22, v194
	v_mul_f32_e32 v22, v115, v26
	v_mul_f32_e32 v115, v22, v191
	v_mul_f32_e32 v22, v107, v26
	v_mul_f32_e32 v107, v22, v195
	v_mul_f32_e32 v22, v116, v26
	v_mul_f32_e32 v116, v22, v192
	v_mul_f32_e32 v22, v108, v26
	v_mul_f32_e32 v108, v22, v196
	v_mul_f32_e32 v22, v117, v26
	v_mul_f32_e32 v117, v22, v193
	v_mul_f32_e32 v22, v109, v26
	v_mul_f32_e32 v109, v22, v197
	s_waitcnt vmcnt(20)
	v_mul_f32_e32 v22, v98, v26
	v_mul_f32_e32 v170, v22, v198
	v_mul_f32_e32 v22, v94, v26
	v_mul_f32_e32 v94, v22, v202
	v_mul_f32_e32 v22, v99, v26
	v_mul_f32_e32 v171, v22, v199
	v_mul_f32_e32 v22, v95, v26
	v_mul_f32_e32 v95, v22, v203
	v_mul_f32_e32 v22, v100, v26
	v_mul_f32_e32 v172, v22, v200
	v_mul_f32_e32 v22, v96, v26
	v_mul_f32_e32 v96, v22, v204
	v_mul_f32_e32 v22, v101, v26
	v_mul_f32_e32 v173, v22, v201
	v_mul_f32_e32 v22, v97, v26
	v_mul_f32_e32 v97, v22, v205
	s_waitcnt vmcnt(18)
	v_mul_f32_e32 v22, v90, v26
	v_mul_f32_e32 v90, v22, v206
	v_mul_f32_e32 v22, v86, v26
	v_mul_f32_e32 v86, v22, v210
	v_mul_f32_e32 v22, v91, v26
	v_mul_f32_e32 v91, v22, v207
	v_mul_f32_e32 v22, v87, v26
	v_mul_f32_e32 v87, v22, v211
	v_mul_f32_e32 v22, v92, v26
	v_mul_f32_e32 v92, v22, v208
	v_mul_f32_e32 v22, v88, v26
	v_mul_f32_e32 v88, v22, v212
	v_mul_f32_e32 v22, v93, v26
	v_mul_f32_e32 v93, v22, v209
	v_mul_f32_e32 v22, v89, v26
	v_mul_f32_e32 v89, v22, v213
	s_waitcnt vmcnt(16)
	v_mul_f32_e32 v22, v78, v26
	v_mul_f32_e32 v78, v22, v214
	v_mul_f32_e32 v22, v74, v26
	v_mul_f32_e32 v74, v22, v218
	v_mul_f32_e32 v22, v79, v26
	v_mul_f32_e32 v79, v22, v215
	v_mul_f32_e32 v22, v75, v26
	v_mul_f32_e32 v75, v22, v219
	v_mul_f32_e32 v22, v80, v26
	v_mul_f32_e32 v80, v22, v216
	v_mul_f32_e32 v22, v76, v26
	v_mul_f32_e32 v76, v22, v220
	v_mul_f32_e32 v22, v81, v26
	v_mul_f32_e32 v81, v22, v217
	v_mul_f32_e32 v22, v77, v26
	v_mul_f32_e32 v77, v22, v221
	s_waitcnt vmcnt(14)
	v_mul_f32_e32 v22, v66, v26
	v_mul_f32_e32 v66, v22, v222
	v_mul_f32_e32 v22, v26, v62
	v_mul_f32_e32 v62, v22, v226
	v_mul_f32_e32 v22, v67, v26
	v_mul_f32_e32 v67, v22, v223
	v_mul_f32_e32 v22, v26, v63
	v_mul_f32_e32 v63, v22, v227
	v_mul_f32_e32 v22, v68, v26
	v_mul_f32_e32 v68, v22, v224
	v_mul_f32_e32 v22, v26, v64
	v_mul_f32_e32 v64, v22, v228
	v_mul_f32_e32 v22, v69, v26
	v_mul_f32_e32 v69, v22, v225
	v_mul_f32_e32 v22, v26, v65
	v_mul_f32_e32 v65, v22, v229
	s_waitcnt vmcnt(12)
	v_mul_f32_e32 v22, v26, v58
	v_mul_f32_e32 v58, v22, v230
	v_mul_f32_e32 v22, v26, v54
	v_mul_f32_e32 v54, v22, v234
	v_mul_f32_e32 v22, v26, v59
	v_mul_f32_e32 v59, v22, v231
	v_mul_f32_e32 v22, v26, v55
	v_mul_f32_e32 v55, v22, v235
	v_mul_f32_e32 v22, v26, v60
	v_mul_f32_e32 v60, v22, v232
	v_mul_f32_e32 v22, v26, v56
	v_mul_f32_e32 v56, v22, v236
	v_mul_f32_e32 v22, v26, v61
	v_mul_f32_e32 v61, v22, v233
	v_mul_f32_e32 v22, v26, v57
	v_mul_f32_e32 v57, v22, v237
	s_waitcnt vmcnt(10)
	v_mul_f32_e32 v22, v26, v50
	v_mul_f32_e32 v174, v22, v238
	v_mul_f32_e32 v22, v26, v46
	v_mul_f32_e32 v175, v22, v242
	v_mul_f32_e32 v22, v26, v51
	v_mul_f32_e32 v176, v22, v239
	v_mul_f32_e32 v22, v26, v47
	v_mul_f32_e32 v177, v22, v243
	v_mul_f32_e32 v22, v26, v52
	v_mul_f32_e32 v52, v22, v240
	v_mul_f32_e32 v22, v26, v48
	v_mul_f32_e32 v180, v22, v244
	v_mul_f32_e32 v22, v26, v53
	v_mul_f32_e32 v53, v22, v241
	v_mul_f32_e32 v22, v26, v49
	v_mul_f32_e32 v181, v22, v245
	s_waitcnt vmcnt(8)
	v_mul_f32_e32 v22, v26, v42
	v_mul_f32_e32 v182, v22, v246
	v_mul_f32_e32 v22, v26, v38
	v_mul_f32_e32 v183, v22, v250
	v_mul_f32_e32 v22, v26, v43
	v_mul_f32_e32 v190, v22, v247
	v_mul_f32_e32 v22, v26, v39
	v_mul_f32_e32 v191, v22, v251
	v_mul_f32_e32 v22, v26, v44
	v_mul_f32_e32 v192, v22, v248
	v_mul_f32_e32 v22, v26, v40
	v_mul_f32_e32 v193, v22, v252
	v_mul_f32_e32 v22, v26, v45
	v_mul_f32_e32 v194, v22, v249
	v_mul_f32_e32 v22, v26, v41
	v_mul_f32_e32 v28, v26, v28
	v_mul_f32_e32 v29, v26, v29
	v_mul_f32_e32 v195, v22, v253
	v_mul_f32_e32 v28, v28, v186
	v_mul_f32_e32 v29, v29, v187
	v_mov_b32_e32 v22, v27
	v_mul_f32_e32 v38, v26, v158
	v_mul_f32_e32 v39, v26, v159
	v_mul_f32_e32 v22, v26, v22
	v_mul_f32_e32 v23, v26, v23
	v_mul_f32_e32 v18, v26, v18
	v_mul_f32_e32 v19, v26, v19
	v_mul_f32_e32 v40, v26, v178
	v_mul_f32_e32 v41, v26, v179
	v_mul_f32_e32 v42, v26, v150
	v_mul_f32_e32 v43, v26, v151
	v_mul_f32_e32 v24, v26, v24
	v_mul_f32_e32 v25, v26, v25
	v_mul_f32_e32 v20, v26, v20
	v_mul_f32_e32 v21, v26, v21
	v_mul_f32_e32 v44, v26, v140
	v_mul_f32_e32 v45, v26, v141
	v_mul_f32_e32 v46, v26, v128
	v_mul_f32_e32 v47, v26, v129
	v_mul_f32_e32 v6, v26, v6
	v_mul_f32_e32 v7, v26, v7
	v_mul_f32_e32 v2, v26, v2
	v_mul_f32_e32 v3, v26, v3
	v_mul_f32_e32 v48, v26, v134
	v_mul_f32_e32 v49, v26, v135
	v_mul_f32_e32 v50, v26, v122
	v_mul_f32_e32 v51, v26, v123
	v_mul_f32_e32 v8, v26, v8
	v_mul_f32_e32 v9, v26, v9
	v_mul_f32_e32 v4, v26, v4
	v_mul_f32_e32 v5, v26, v5
	s_waitcnt vmcnt(4)
	v_mul_f32_e32 v26, v29, v34
	v_mul_f32_e32 v27, v28, v35
	v_mul_f32_e32 v22, v22, v188
	v_mul_f32_e32 v23, v23, v189
	v_mul_f32_e32 v48, v48, v130
	v_mul_f32_e32 v49, v49, v131
	v_sub_f32_e32 v130, v26, v27
	v_mul_f32_e32 v26, v28, v34
	v_mul_f32_e32 v27, v29, v35
	v_mul_f32_e32 v40, v40, v156
	v_mul_f32_e32 v41, v41, v157
	v_add_f32_e32 v28, v27, v26
	v_mul_f32_e32 v26, v23, v36
	v_mul_f32_e32 v27, v22, v37
	v_mul_f32_e32 v22, v22, v36
	v_mul_f32_e32 v23, v23, v37
	v_sub_f32_e32 v26, v26, v27
	v_add_f32_e32 v27, v23, v22
	v_mul_f32_e32 v22, v41, v30
	v_mul_f32_e32 v23, v40, v31
	v_mul_f32_e32 v24, v24, v184
	v_mul_f32_e32 v25, v25, v185
	v_sub_f32_e32 v29, v22, v23
	v_mul_f32_e32 v22, v40, v30
	v_mul_f32_e32 v23, v41, v31
	v_mul_f32_e32 v38, v38, v152
	v_mul_f32_e32 v39, v39, v153
	v_add_f32_e32 v30, v23, v22
	v_mul_f32_e32 v22, v25, v32
	v_mul_f32_e32 v23, v24, v33
	v_sub_f32_e32 v31, v22, v23
	v_mul_f32_e32 v22, v24, v32
	v_mul_f32_e32 v23, v25, v33
	v_mul_f32_e32 v18, v18, v154
	v_mul_f32_e32 v19, v19, v155
	v_add_f32_e32 v24, v23, v22
	v_mul_f32_e32 v22, v39, v14
	v_mul_f32_e32 v23, v38, v15
	v_mul_f32_e32 v14, v38, v14
	v_mul_f32_e32 v15, v39, v15
	v_sub_f32_e32 v22, v22, v23
	v_add_f32_e32 v23, v15, v14
	v_mul_f32_e32 v14, v19, v16
	v_mul_f32_e32 v15, v18, v17
	v_mul_f32_e32 v42, v42, v142
	v_mul_f32_e32 v43, v43, v143
	v_sub_f32_e32 v25, v14, v15
	v_mul_f32_e32 v14, v18, v16
	v_mul_f32_e32 v15, v19, v17
	v_mul_f32_e32 v20, v20, v144
	v_mul_f32_e32 v21, v21, v145
	v_add_f32_e32 v16, v15, v14
	v_mul_f32_e32 v14, v43, v10
	v_mul_f32_e32 v15, v42, v11
	v_mul_f32_e32 v10, v42, v10
	v_mul_f32_e32 v11, v43, v11
	v_sub_f32_e32 v14, v14, v15
	v_add_f32_e32 v15, v11, v10
	v_mul_f32_e32 v10, v21, v12
	v_mul_f32_e32 v11, v20, v13
	v_mul_f32_e32 v44, v44, v136
	v_mul_f32_e32 v45, v45, v137
	v_sub_f32_e32 v17, v10, v11
	v_mul_f32_e32 v10, v20, v12
	v_mul_f32_e32 v11, v21, v13
	v_mul_f32_e32 v6, v6, v138
	v_mul_f32_e32 v7, v7, v139
	v_add_f32_e32 v12, v11, v10
	s_waitcnt vmcnt(0)
	v_mul_f32_e32 v10, v45, v110
	v_mul_f32_e32 v11, v44, v111
	v_sub_f32_e32 v13, v10, v11
	v_mul_f32_e32 v10, v44, v110
	v_mul_f32_e32 v11, v45, v111
	v_mul_f32_e32 v8, v8, v132
	v_mul_f32_e32 v9, v9, v133
	v_add_f32_e32 v18, v11, v10
	v_mul_f32_e32 v10, v7, v112
	v_mul_f32_e32 v11, v6, v113
	v_mul_f32_e32 v6, v6, v112
	v_mul_f32_e32 v7, v7, v113
	v_sub_f32_e32 v10, v10, v11
	v_add_f32_e32 v11, v7, v6
	v_mul_f32_e32 v6, v49, v102
	v_mul_f32_e32 v7, v48, v103
	v_sub_f32_e32 v19, v6, v7
	v_mul_f32_e32 v6, v48, v102
	v_mul_f32_e32 v7, v49, v103
	v_mul_f32_e32 v46, v46, v124
	v_mul_f32_e32 v47, v47, v125
	v_add_f32_e32 v20, v7, v6
	v_mul_f32_e32 v6, v9, v104
	v_mul_f32_e32 v7, v8, v105
	v_sub_f32_e32 v21, v6, v7
	v_mul_f32_e32 v6, v8, v104
	v_mul_f32_e32 v7, v9, v105
	v_mul_f32_e32 v2, v2, v126
	v_mul_f32_e32 v3, v3, v127
	v_add_f32_e32 v8, v7, v6
	v_mul_f32_e32 v6, v47, v82
	v_mul_f32_e32 v7, v46, v83
	v_sub_f32_e32 v9, v6, v7
	v_mul_f32_e32 v6, v46, v82
	v_mul_f32_e32 v7, v47, v83
	v_mul_f32_e32 v50, v50, v118
	v_mul_f32_e32 v51, v51, v119
	v_add_f32_e32 v32, v7, v6
	v_mul_f32_e32 v6, v3, v84
	v_mul_f32_e32 v7, v2, v85
	v_mul_f32_e32 v2, v2, v84
	v_mul_f32_e32 v3, v3, v85
	v_sub_f32_e32 v6, v6, v7
	v_add_f32_e32 v7, v3, v2
	v_mul_f32_e32 v2, v51, v70
	v_mul_f32_e32 v3, v50, v71
	v_mul_f32_e32 v4, v4, v120
	v_mul_f32_e32 v5, v5, v121
	v_sub_f32_e32 v33, v2, v3
	v_mul_f32_e32 v2, v50, v70
	v_mul_f32_e32 v3, v51, v71
	v_cvt_pk_bf16_f32 v98, v114, v115
	v_cvt_pk_bf16_f32 v99, v116, v117
	v_cvt_pk_bf16_f32 v100, v106, v107
	v_cvt_pk_bf16_f32 v101, v108, v109
	v_cvt_pk_bf16_f32 v102, v170, v171
	s_nop 0
	v_add_f32_e32 v34, v3, v2
	v_mul_f32_e32 v2, v5, v72
	v_mul_f32_e32 v3, v4, v73
	v_sub_f32_e32 v35, v2, v3
	v_mul_f32_e32 v2, v4, v72
	v_mul_f32_e32 v3, v5, v73
	v_cvt_pk_bf16_f32 v103, v172, v173
	v_cvt_pk_bf16_f32 v104, v94, v95
	v_cvt_pk_bf16_f32 v105, v96, v97
	v_cvt_pk_bf16_f32 v106, v90, v91
	v_cvt_pk_bf16_f32 v107, v92, v93
	s_nop 0
	v_add_f32_e32 v2, v3, v2
	v_cvt_pk_bf16_f32 v108, v86, v87
	v_cvt_pk_bf16_f32 v109, v88, v89
	v_cvt_pk_bf16_f32 v110, v78, v79
	v_cvt_pk_bf16_f32 v111, v80, v81
	v_cvt_pk_bf16_f32 v112, v74, v75
	v_cvt_pk_bf16_f32 v113, v76, v77
	v_cvt_pk_bf16_f32 v114, v66, v67
	v_cvt_pk_bf16_f32 v115, v68, v69
	v_cvt_pk_bf16_f32 v116, v62, v63
	v_cvt_pk_bf16_f32 v117, v64, v65
	v_cvt_pk_bf16_f32 v118, v58, v59
	v_cvt_pk_bf16_f32 v119, v60, v61
	v_cvt_pk_bf16_f32 v120, v54, v55
	v_cvt_pk_bf16_f32 v121, v56, v57
	v_cvt_pk_bf16_f32 v122, v174, v176
	v_cvt_pk_bf16_f32 v123, v52, v53
	v_cvt_pk_bf16_f32 v124, v175, v177
	v_cvt_pk_bf16_f32 v125, v180, v181
	v_cvt_pk_bf16_f32 v126, v182, v190
	v_cvt_pk_bf16_f32 v127, v192, v194
	v_cvt_pk_bf16_f32 v128, v183, v191
	v_cvt_pk_bf16_f32 v129, v193, v195
	v_cvt_pk_bf16_f32 v130, v130, v26
	v_cvt_pk_bf16_f32 v131, v29, v31
	v_cvt_pk_bf16_f32 v132, v22, v25
	v_cvt_pk_bf16_f32 v133, v14, v17
	v_cvt_pk_bf16_f32 v134, v13, v10
	v_cvt_pk_bf16_f32 v135, v19, v21
	v_cvt_pk_bf16_f32 v136, v9, v6
	v_cvt_pk_bf16_f32 v137, v33, v35
	v_cvt_pk_bf16_f32 v138, v28, v27
	v_cvt_pk_bf16_f32 v139, v30, v24
	v_cvt_pk_bf16_f32 v140, v23, v16
	v_cvt_pk_bf16_f32 v141, v15, v12
	v_cvt_pk_bf16_f32 v142, v18, v11
	v_cvt_pk_bf16_f32 v143, v20, v8
	v_cvt_pk_bf16_f32 v144, v32, v7
	v_cvt_pk_bf16_f32 v145, v34, v2
	v_mul_hi_i32 v2, v168, s70
	v_lshrrev_b32_e32 v3, 31, v2
	v_ashrrev_i32_e32 v2, 2, v2
	v_add_u32_e32 v2, v2, v3
	v_mul_lo_u32 v3, v2, 24
	v_sub_u32_e32 v3, v168, v3
	v_lshrrev_b32_e32 v16, 1, v2
	v_bitop3_b32 v3, v16, v3, 7 bitop3:0x6c
	v_mul_lo_u32 v2, v2, s68
	v_lshl_add_u32 v2, v3, 4, v2
	v_add_u32_e32 v3, 0x200, v168
	v_mul_hi_i32 v4, v3, s70
	v_lshrrev_b32_e32 v5, 31, v4
	v_ashrrev_i32_e32 v4, 2, v4
	v_add_u32_e32 v4, v4, v5
	v_mul_lo_u32 v5, v4, 24
	v_sub_u32_e32 v5, v3, v5
	v_lshrrev_b32_e32 v16, 1, v4
	v_bitop3_b32 v5, v16, v5, 7 bitop3:0x6c
	v_mul_lo_u32 v4, v4, s68
	v_lshl_add_u32 v4, v5, 4, v4
	v_add_u32_e32 v5, 0x400, v168
	v_mul_hi_i32 v6, v5, s70
	v_lshrrev_b32_e32 v7, 31, v6
	v_ashrrev_i32_e32 v6, 2, v6
	v_add_u32_e32 v6, v6, v7
	v_mul_lo_u32 v7, v6, 24
	v_sub_u32_e32 v5, v5, v7
	v_lshrrev_b32_e32 v16, 1, v6
	v_bitop3_b32 v5, v16, v5, 7 bitop3:0x6c
	v_mul_lo_u32 v6, v6, s68
	v_ashrrev_i32_e32 v9, 4, v168
	v_lshl_add_u32 v6, v5, 4, v6
	v_bfe_u32 v5, v168, 2, 2
	v_lshrrev_b32_e32 v7, 1, v168
	v_and_b32_e32 v10, 0x1ffff0, v9
	v_lshrrev_b32_e32 v9, 1, v9
	v_ashrrev_i32_e32 v3, 4, v3
	v_and_or_b32 v5, v7, 8, v5
	v_and_b32_e32 v7, 0x60, v168
	v_lshlrev_b32_e32 v8, 3, v168
	v_and_b32_e32 v9, 4, v9
	v_and_b32_e32 v11, 0x1ffff0, v3
	v_lshrrev_b32_e32 v3, 1, v3
	v_and_or_b32 v7, v8, 24, v7
	v_or3_b32 v9, v10, v9, v5
	v_and_b32_e32 v3, 4, v3


	v_lshlrev_b32_e32 v7, 1, v7
	v_lshlrev_b32_e32 v10, 11, v9
	v_or3_b32 v3, v11, v3, v5


	v_or_b32_e32 v9, v10, v7
	v_lshlrev_b32_e32 v11, 11, v3


	v_or_b32_e32 v3, v11, v7


	v_lshlrev_b32_e32 v13, 1, v168

	v_lshlrev_b32_e32 v9, 4, v168
	v_and_b32_e32 v14, 32, v13
	v_or_b32_e32 v3, 32, v148
	v_and_b32_e32 v16, 0x13, v167
	v_and_b32_e32 v17, 4, v167
	v_lshl_or_b32 v16, v17, 1, v16
	v_and_b32_e32 v17, 8, v167
	v_lshrrev_b32_e32 v17, 1, v17
	v_or_b32_e32 v16, v16, v17
	v_mul_u32_u24_e32 v5, 0x180, v16
	v_lshlrev_b32_e32 v17, 3, v16
	v_and_b32_e32 v7, 0x70, v17
	v_and_b32_e32 v12, 0xc0, v9
	v_and_or_b32 v8, v8, s75, v14
	v_bitop3_b32 v172, v3, v5, v7 bitop3:0xde
	v_or_b32_e32 v3, 64, v148
	v_mul_i32_i24_e32 v15, -8, v169
	v_add3_u32 v169, v12, 0, v8
	v_and_b32_e32 v12, 0xc0, v13
	v_and_b32_e32 v13, 48, v9
	v_bitop3_b32 v173, v3, v5, v7 bitop3:0xde
	v_or_b32_e32 v3, 0x60, v148
	v_or3_b32 v8, v11, v12, v13
	v_mov_b32_e32 v9, v149
	v_bitop3_b32 v171, v148, v5, v7 bitop3:0xde
	v_bitop3_b32 v174, v3, v5, v7 bitop3:0xde
	v_mov_b32_e32 v3, v149
	v_mov_b32_e32 v5, v149
	v_mov_b32_e32 v7, v149
	v_lshl_add_u64 v[150:151], s[48:49], 0, v[8:9]
	v_mov_b32_e32 v240, v8
	v_or3_b32 v8, v10, v12, v13
	v_mov_b32_e32 v16, v149
	v_mov_b32_e32 v17, v149
	v_and_b32_e32 v170, 63, v168
	s_lshl_b32 s46, s80, 2
	v_lshl_add_u32 v168, v167, 2, s65
	v_lshl_add_u64 v[152:153], s[48:49], 0, v[8:9]
	v_mov_b32_e32 v241, v8
	v_lshl_add_u64 v[154:155], s[50:51], 0, v[6:7]
	v_mov_b32_e32 v242, v6
	v_lshl_add_u64 v[156:157], s[50:51], 0, v[4:5]
	v_mov_b32_e32 v243, v4
	v_lshl_add_u64 v[158:159], s[50:51], 0, v[2:3]
	v_mov_b32_e32 v244, v2
	s_add_u32 s94, s2, s50
	s_addc_u32 s95, s3, s51
	s_add_u32 s96, s2, s48
	s_addc_u32 s97, s3, s49
	v_add3_u32 v167, s63, v15, v167
	v_mov_b32_e32 v2, v149
	v_mov_b32_e32 v4, v149
	v_mov_b32_e32 v6, v149
	v_mov_b32_e32 v8, v149
	v_mov_b32_e32 v10, v149
	v_mov_b32_e32 v11, v149
	v_mov_b32_e32 v12, v149
	v_mov_b32_e32 v13, v149
	v_mov_b32_e32 v14, v149
	v_mov_b32_e32 v15, v149
	v_mov_b64_e32 v[32:33], v[16:17]
	v_mov_b64_e32 v[48:49], v[16:17]
	v_mov_b64_e32 v[64:65], v[16:17]
	s_add_i32 s46, s46, 4
	v_cmp_gt_u32_e64 s[0:1], 32, v170
	v_mov_b32_e32 v176, 0
	v_mov_b32_e32 v175, 0
	v_mov_b32_e32 v210, 0
	v_mov_b32_e32 v211, 0
	v_mov_b32_e32 v212, 0
	v_mov_b32_e32 v213, 0
	v_mov_b32_e32 v214, 0
	v_mov_b32_e32 v215, 0
	v_mov_b32_e32 v216, 0
	v_mov_b32_e32 v217, 0
	v_mov_b32_e32 v218, 0
	v_mov_b32_e32 v219, 0
	v_mov_b32_e32 v220, 0
	v_mov_b32_e32 v221, 0
	v_mov_b32_e32 v222, 0
	v_mov_b32_e32 v223, 0
	v_mov_b32_e32 v224, 0
	v_mov_b32_e32 v225, 0
	s_movk_i32 s47, 0xff00
	v_mov_b64_e32 v[30:31], v[14:15]
	v_mov_b64_e32 v[28:29], v[12:13]
	v_mov_b64_e32 v[26:27], v[10:11]
	v_mov_b64_e32 v[24:25], v[8:9]
	v_mov_b64_e32 v[22:23], v[6:7]
	v_mov_b64_e32 v[20:21], v[4:5]
	v_mov_b64_e32 v[18:19], v[2:3]
	v_mov_b64_e32 v[46:47], v[14:15]
	v_mov_b64_e32 v[44:45], v[12:13]
	v_mov_b64_e32 v[42:43], v[10:11]
	v_mov_b64_e32 v[40:41], v[8:9]
	v_mov_b64_e32 v[38:39], v[6:7]
	v_mov_b64_e32 v[36:37], v[4:5]
	v_mov_b64_e32 v[34:35], v[2:3]
	v_mov_b64_e32 v[62:63], v[14:15]
	v_mov_b64_e32 v[60:61], v[12:13]
	v_mov_b64_e32 v[58:59], v[10:11]
	v_mov_b64_e32 v[56:57], v[8:9]
	v_mov_b64_e32 v[54:55], v[6:7]
	v_mov_b64_e32 v[52:53], v[4:5]
	v_mov_b64_e32 v[50:51], v[2:3]
	s_cmp_ge_u32 s64, 0x1000
	s_cbranch_scc0 .Lprio_skip_a2
	s_setprio 1
